# speedup vs baseline: 1.0054x; 1.0054x over previous
.LBB11_9:
	s_or_b64 exec, exec, s[12:13]
	s_and_saveexec_b64 s[4:5], s[6:7]
	v_mov_b32_e32 v1, 0x21200
	v_lshl_add_u32 v0, v0, 2, v1
	ds_write_b32 v0, v5
	s_or_b64 exec, exec, s[4:5]
	s_movk_i32 s3, 0x7e90
	v_cmp_gt_i32_e32 vcc, s3, v9
	s_waitcnt lgkmcnt(0)
	s_barrier
	s_and_saveexec_b64 s[4:5], vcc
	s_cbranch_execz .LBB11_16
	v_lshlrev_b32_e32 v94, 5, v164
	v_or_b32_e32 v0, 0x1f800, v94
	v_or_b32_e32 v4, 0x1fa00, v94
	v_cvt_f32_i32_e32 v9, v8
	v_cvt_f32_i32_e32 v8, v2
	ds_read_b128 v[0:3], v0
	ds_read_b128 v[4:7], v4
	v_lshlrev_b32_e32 v165, 4, v164
	s_movk_i32 s3, 0x110
	v_pk_add_f32 v[92:93], v[8:9], 0.5 op_sel_hi:[1,0]
	s_waitcnt lgkmcnt(1)
	v_mov_b32_e32 v8, v0
	s_waitcnt lgkmcnt(0)
	v_mov_b32_e32 v9, v4
	v_or_b32_e32 v0, 0x1fc00, v94
	v_pk_mul_f32 v[20:21], v[92:93], v[8:9]
	v_or_b32_e32 v4, 0x1fe00, v94
	ds_read_b128 v[8:11], v0
	ds_read_b128 v[12:15], v4
	v_or_b32_e32 v0, 0x20000, v94
	ds_read_b128 v[16:19], v0
	v_add_f32_e32 v0, v20, v21
	s_waitcnt lgkmcnt(2)
	v_add_f32_e32 v0, v8, v0
	v_or_b32_e32 v4, 0x1f810, v94
	ds_read_b128 v[20:23], v4
	s_waitcnt lgkmcnt(1)
	v_fma_f32 v0, v12, v0, v16
	v_mov_b32_e32 v4, v1
	v_max_f32_e32 v24, 0, v0
	v_pk_mul_f32 v[0:1], v[92:93], v[4:5]
	v_or_b32_e32 v4, 0x1fc10, v94
	v_add_f32_e32 v0, v0, v1
	v_add_f32_e32 v0, v9, v0
	v_fma_f32 v0, v13, v0, v17
	v_max_f32_e32 v25, 0, v0
	v_mov_b32_e32 v0, v2
	v_mov_b32_e32 v1, v6
	v_pk_mul_f32 v[0:1], v[92:93], v[0:1]
	v_mov_b32_e32 v6, v3
	v_add_f32_e32 v0, v0, v1
	v_add_f32_e32 v0, v10, v0
	v_fma_f32 v0, v14, v0, v18
	v_max_f32_e32 v18, 0, v0
	v_pk_mul_f32 v[0:1], v[92:93], v[6:7]
	v_or_b32_e32 v8, 0x1fe10, v94
	v_add_f32_e32 v0, v0, v1
	v_add_f32_e32 v0, v11, v0
	v_fmac_f32_e32 v19, v15, v0
	v_or_b32_e32 v0, 0x1fa10, v94
	ds_read_b128 v[0:3], v0
	ds_read_b128 v[4:7], v4
	v_or_b32_e32 v12, 0x20010, v94
	ds_read_b128 v[8:11], v8
	ds_read_b128 v[12:15], v12
	s_waitcnt lgkmcnt(4)
	v_mov_b32_e32 v16, v20
	s_waitcnt lgkmcnt(3)
	v_mov_b32_e32 v17, v0
	v_pk_mul_f32 v[16:17], v[92:93], v[16:17]
	v_mad_u32_u24 v166, v145, s3, v165
	v_add_f32_e32 v0, v16, v17
	s_waitcnt lgkmcnt(2)
	v_add_f32_e32 v0, v4, v0
	s_waitcnt lgkmcnt(0)
	v_fma_f32 v0, v8, v0, v12
	v_max_f32_e32 v4, 0, v0
	v_mov_b32_e32 v0, v21
	v_pk_mul_f32 v[0:1], v[92:93], v[0:1]
	v_max_f32_e32 v19, 0, v19
	v_add_f32_e32 v0, v0, v1
	v_add_f32_e32 v0, v5, v0
	v_fma_f32 v0, v9, v0, v13
	v_max_f32_e32 v5, 0, v0
	v_mov_b32_e32 v0, v22
	v_mov_b32_e32 v1, v2
	v_pk_mul_f32 v[0:1], v[92:93], v[0:1]
	v_mov_b32_e32 v2, v23
	v_add_f32_e32 v0, v0, v1
	v_add_f32_e32 v0, v6, v0
	v_fma_f32 v0, v10, v0, v14
	v_max_f32_e32 v6, 0, v0
	v_pk_mul_f32 v[0:1], v[92:93], v[2:3]
	ds_read_b128 v[96:99], v166 offset:32
	v_add_f32_e32 v8, v0, v1
	ds_read_b128 v[0:3], v166
	v_add_f32_e32 v7, v7, v8
	v_fmac_f32_e32 v15, v11, v7
	v_max_f32_e32 v7, 0, v15
	v_cvt_pk_f16_f32 v7, v6, v7
	v_cvt_pk_f16_f32 v6, v4, v5
	v_cvt_pk_f16_f32 v5, v18, v19
	v_cvt_pk_f16_f32 v4, v24, v25
	v_or_b32_e32 v8, 0x1f840, v94
	v_or_b32_e32 v9, 0x1fa40, v94
	s_waitcnt lgkmcnt(0)
	v_mfma_f32_32x32x16_f16 v[48:63], v[0:3], v[4:7], 0
	v_mov_b32_e32 v190, 0x8180
	v_mad_i64_i32 v[192:193], s[40:41], s36, v190, v[198:199]
	v_lshlrev_b64 v[192:193], 6, v[192:193]
	v_lshl_add_u64 v[196:197], s[38:39], 0, v[192:193]
	v_mov_b32_e32 v193, 0
	v_lshlrev_b32_e32 v192, 3, v164
	v_lshl_add_u64 v[196:197], v[196:197], 0, v[192:193]
	global_load_dwordx2 v[90:91], v[196:197], off
	global_load_dwordx2 v[88:89], v[196:197], off offset:32
	global_load_dwordx2 v[84:85], v[196:197], off offset:48
	global_load_dwordx2 v[86:87], v[196:197], off offset:16
	ds_read_b128 v[0:3], v166 offset:8704
	ds_read_b128 v[100:103], v166 offset:8736
	v_or_b32_e32 v95, 0x1fc40, v94
	s_mov_b32 s4, 0x3a000000
	s_ashr_i32 s37, s36, 31
	s_waitcnt lgkmcnt(1)
	v_mfma_f32_32x32x16_f16 v[32:47], v[0:3], v[4:7], 0
	v_mad_i64_i32 v[196:197], s[40:41], s34, v190, v[198:199]
	v_lshlrev_b64 v[196:197], 6, v[196:197]
	v_lshl_add_u64 v[196:197], s[38:39], 0, v[196:197]
	v_lshl_add_u64 v[196:197], v[196:197], 0, v[192:193]
	global_load_dwordx2 v[82:83], v[196:197], off
	global_load_dwordx2 v[80:81], v[196:197], off offset:32
	global_load_dwordx2 v[76:77], v[196:197], off offset:48
	global_load_dwordx2 v[78:79], v[196:197], off offset:16
	ds_read_b128 v[0:3], v166 offset:17408
	ds_read_b128 v[104:107], v166 offset:17440
	s_ashr_i32 s35, s34, 31
	s_ashr_i32 s31, s30, 31
	s_ashr_i32 s29, s28, 31
	s_ashr_i32 s27, s26, 31
	s_ashr_i32 s25, s24, 31
	s_ashr_i32 s11, s10, 31
	s_waitcnt lgkmcnt(1)
	v_mfma_f32_32x32x16_f16 v[16:31], v[0:3], v[4:7], 0
	v_mad_i64_i32 v[196:197], s[40:41], s30, v190, v[198:199]
	v_lshlrev_b64 v[196:197], 6, v[196:197]
	v_lshl_add_u64 v[196:197], s[38:39], 0, v[196:197]
	v_lshl_add_u64 v[196:197], v[196:197], 0, v[192:193]
	global_load_dwordx2 v[74:75], v[196:197], off
	global_load_dwordx2 v[72:73], v[196:197], off offset:32
	global_load_dwordx2 v[68:69], v[196:197], off offset:48
	global_load_dwordx2 v[70:71], v[196:197], off offset:16
	ds_read_b128 v[0:3], v166 offset:26112
	ds_read_b128 v[108:111], v8
	ds_read_b128 v[112:115], v9
	ds_read_b128 v[116:119], v166 offset:26144
	s_ashr_i32 s3, s2, 31
	s_waitcnt lgkmcnt(2)
	v_mov_b32_e32 v120, v108
	s_waitcnt lgkmcnt(1)
	v_mov_b32_e32 v121, v112
	v_pk_mul_f32 v[124:125], v[92:93], v[120:121]
	v_or_b32_e32 v108, 0x1fe40, v94
	ds_read_b128 v[120:123], v95
	ds_read_b128 v[168:171], v108
	v_or_b32_e32 v95, 0x20040, v94
	ds_read_b128 v[172:175], v95
	v_or_b32_e32 v108, 0x1f850, v94
	v_mov_b32_e32 v112, v109
	ds_read_b128 v[176:179], v108
	v_pk_mul_f32 v[108:109], v[92:93], v[112:113]
	v_add_f32_e32 v95, v124, v125
	v_add_f32_e32 v108, v108, v109
	s_waitcnt lgkmcnt(3)
	v_add_f32_e32 v108, v121, v108
	s_waitcnt lgkmcnt(1)
	v_fma_f32 v108, v169, v108, v173
	v_max_f32_e32 v167, 0, v108
	v_mov_b32_e32 v108, v110
	v_mov_b32_e32 v109, v114
	v_pk_mul_f32 v[108:109], v[92:93], v[108:109]
	v_add_f32_e32 v95, v120, v95
	v_add_f32_e32 v108, v108, v109
	v_add_f32_e32 v108, v122, v108
	v_fma_f32 v108, v170, v108, v174
	v_mov_b32_e32 v114, v111
	v_fma_f32 v95, v168, v95, v172
	v_max_f32_e32 v172, 0, v108
	v_pk_mul_f32 v[108:109], v[92:93], v[114:115]
	v_or_b32_e32 v112, 0x1fc50, v94
	v_add_f32_e32 v108, v108, v109
	v_add_f32_e32 v108, v123, v108
	v_fmac_f32_e32 v175, v171, v108
	v_or_b32_e32 v108, 0x1fa50, v94
	ds_read_b128 v[108:111], v108
	ds_read_b128 v[112:115], v112
	v_or_b32_e32 v120, 0x1fe50, v94
	v_or_b32_e32 v125, 0x20050, v94
	ds_read_b128 v[120:123], v120
	ds_read_b128 v[168:171], v125
	s_waitcnt lgkmcnt(4)
	v_mov_b32_e32 v124, v176
	s_waitcnt lgkmcnt(3)
	v_mov_b32_e32 v125, v108
	v_pk_mul_f32 v[124:125], v[92:93], v[124:125]
	v_max_f32_e32 v95, 0, v95
	v_add_f32_e32 v108, v124, v125
	s_waitcnt lgkmcnt(2)
	v_add_f32_e32 v108, v112, v108
	s_waitcnt lgkmcnt(0)
	v_fma_f32 v108, v120, v108, v168
	v_max_f32_e32 v112, 0, v108
	v_mov_b32_e32 v108, v177
	v_pk_mul_f32 v[108:109], v[92:93], v[108:109]
	v_max_f32_e32 v173, 0, v175
	v_add_f32_e32 v108, v108, v109
	v_add_f32_e32 v108, v113, v108
	v_fma_f32 v108, v121, v108, v169
	v_max_f32_e32 v113, 0, v108
	v_mov_b32_e32 v108, v178
	v_mov_b32_e32 v109, v110
	v_pk_mul_f32 v[108:109], v[92:93], v[108:109]
	v_mov_b32_e32 v110, v179
	v_add_f32_e32 v108, v108, v109
	v_add_f32_e32 v108, v114, v108
	v_fma_f32 v108, v122, v108, v170
	v_max_f32_e32 v114, 0, v108
	v_pk_mul_f32 v[108:109], v[92:93], v[110:111]
	v_mfma_f32_32x32x16_f16 v[0:15], v[0:3], v[4:7], 0
	v_mad_i64_i32 v[196:197], s[40:41], s28, v190, v[198:199]
	v_lshlrev_b64 v[196:197], 6, v[196:197]
	v_lshl_add_u64 v[196:197], s[38:39], 0, v[196:197]
	v_lshl_add_u64 v[196:197], v[196:197], 0, v[192:193]
	global_load_dwordx2 v[66:67], v[196:197], off
	global_load_dwordx2 v[64:65], v[196:197], off offset:32
	global_load_dwordx2 v[126:127], v[196:197], off offset:48
	global_load_dwordx2 v[162:163], v[196:197], off offset:16
	v_add_f32_e32 v108, v108, v109
	v_add_f32_e32 v108, v115, v108
	v_fmac_f32_e32 v171, v123, v108
	v_max_f32_e32 v108, 0, v171
	v_cvt_pk_f16_f32 v111, v114, v108
	v_cvt_pk_f16_f32 v110, v112, v113
	v_cvt_pk_f16_f32 v109, v172, v173
	v_cvt_pk_f16_f32 v108, v95, v167
	v_or_b32_e32 v95, 0x1f880, v94
	s_nop 0
	v_mfma_f32_32x32x16_f16 v[32:47], v[100:103], v[108:111], v[32:47]
	v_mad_i64_i32 v[196:197], s[40:41], s26, v190, v[198:199]
	v_lshlrev_b64 v[196:197], 6, v[196:197]
	v_lshl_add_u64 v[196:197], s[38:39], 0, v[196:197]
	v_lshl_add_u64 v[196:197], v[196:197], 0, v[192:193]
	global_load_dwordx2 v[160:161], v[196:197], off
	global_load_dwordx2 v[128:129], v[196:197], off offset:32
	global_load_dwordx2 v[130:131], v[196:197], off offset:48
	global_load_dwordx2 v[158:159], v[196:197], off offset:16
	v_or_b32_e32 v100, 0x1fa80, v94
	v_mfma_f32_32x32x16_f16 v[48:63], v[96:99], v[108:111], v[48:63]
	v_mad_i64_i32 v[196:197], s[40:41], s24, v190, v[198:199]
	v_lshlrev_b64 v[196:197], 6, v[196:197]
	v_lshl_add_u64 v[196:197], s[38:39], 0, v[196:197]
	v_lshl_add_u64 v[196:197], v[196:197], 0, v[192:193]
	global_load_dwordx2 v[156:157], v[196:197], off
	global_load_dwordx2 v[132:133], v[196:197], off offset:32
	global_load_dwordx2 v[134:135], v[196:197], off offset:48
	global_load_dwordx2 v[154:155], v[196:197], off offset:16
	ds_read_b128 v[96:99], v95
	ds_read_b128 v[100:103], v100
	v_or_b32_e32 v95, 0x1fc80, v94
	v_mfma_f32_32x32x16_f16 v[16:31], v[104:107], v[108:111], v[16:31]
	v_mad_i64_i32 v[196:197], s[40:41], s10, v190, v[198:199]
	v_mad_i64_i32 v[198:199], s[40:41], s2, v190, v[198:199]
	v_lshlrev_b64 v[196:197], 6, v[196:197]
	v_lshlrev_b64 v[198:199], 6, v[198:199]
	v_lshl_add_u64 v[196:197], s[38:39], 0, v[196:197]
	v_lshl_add_u64 v[198:199], s[38:39], 0, v[198:199]
	v_lshl_add_u64 v[196:197], v[196:197], 0, v[192:193]
	v_lshl_add_u64 v[198:199], v[198:199], 0, v[192:193]
	global_load_dwordx2 v[152:153], v[196:197], off
	global_load_dwordx2 v[136:137], v[196:197], off offset:32
	global_load_dwordx2 v[138:139], v[196:197], off offset:48
	global_load_dwordx2 v[150:151], v[196:197], off offset:16
	global_load_dwordx2 v[148:149], v[198:199], off
	global_load_dwordx2 v[140:141], v[198:199], off offset:32
	global_load_dwordx2 v[142:143], v[198:199], off offset:48
	global_load_dwordx2 v[146:147], v[198:199], off offset:16
	s_waitcnt lgkmcnt(1)
	v_mov_b32_e32 v104, v96
	s_waitcnt lgkmcnt(0)
	v_mov_b32_e32 v105, v100
	v_or_b32_e32 v96, 0x1fe80, v94
	v_mov_b32_e32 v100, v97
	v_mfma_f32_32x32x16_f16 v[0:15], v[116:119], v[108:111], v[0:15]
	v_mul_f32_e64 v116, v92, v104
	v_mul_f32_e64 v117, v93, v105
	ds_read_b128 v[104:107], v95
	ds_read_b128 v[108:111], v96
	v_or_b32_e32 v95, 0x20080, v94
	ds_read_b128 v[112:115], v95
	v_or_b32_e32 v96, 0x1f890, v94
	v_add_f32_e32 v95, v116, v117
	ds_read_b128 v[116:119], v96
	v_pk_mul_f32 v[96:97], v[92:93], v[100:101]
	v_or_b32_e32 v100, 0x1fc90, v94
	v_add_f32_e32 v96, v96, v97
	s_waitcnt lgkmcnt(3)
	v_add_f32_e32 v96, v105, v96
	s_waitcnt lgkmcnt(1)
	v_fma_f32 v96, v109, v96, v113
	v_max_f32_e32 v120, 0, v96
	v_mov_b32_e32 v96, v98
	v_mov_b32_e32 v97, v102
	v_pk_mul_f32 v[96:97], v[92:93], v[96:97]
	v_mov_b32_e32 v102, v99
	v_add_f32_e32 v96, v96, v97
	v_add_f32_e32 v96, v106, v96
	v_fma_f32 v96, v110, v96, v114
	v_max_f32_e32 v114, 0, v96
	v_pk_mul_f32 v[96:97], v[92:93], v[102:103]
	v_add_f32_e32 v95, v104, v95
	v_add_f32_e32 v96, v96, v97
	v_add_f32_e32 v96, v107, v96
	v_fmac_f32_e32 v115, v111, v96
	v_or_b32_e32 v96, 0x1fa90, v94
	ds_read_b128 v[96:99], v96
	ds_read_b128 v[100:103], v100
	v_fma_f32 v95, v108, v95, v112
	v_or_b32_e32 v104, 0x1fe90, v94
	v_or_b32_e32 v108, 0x20090, v94
	ds_read_b128 v[104:107], v104
	ds_read_b128 v[108:111], v108
	s_waitcnt lgkmcnt(4)
	v_mov_b32_e32 v112, v116
	s_waitcnt lgkmcnt(3)
	v_mov_b32_e32 v113, v96
	v_pk_mul_f32 v[112:113], v[92:93], v[112:113]
	v_max_f32_e32 v95, 0, v95
	v_add_f32_e32 v96, v112, v113
	s_waitcnt lgkmcnt(2)
	v_add_f32_e32 v96, v100, v96
	s_waitcnt lgkmcnt(0)
	v_fma_f32 v96, v104, v96, v108
	v_max_f32_e32 v100, 0, v96
	v_mov_b32_e32 v96, v117
	v_pk_mul_f32 v[96:97], v[92:93], v[96:97]
	v_max_f32_e32 v115, 0, v115
	v_add_f32_e32 v96, v96, v97
	v_add_f32_e32 v96, v101, v96
	v_fma_f32 v96, v105, v96, v109
	v_max_f32_e32 v101, 0, v96
	v_mov_b32_e32 v96, v118
	v_mov_b32_e32 v97, v98
	v_pk_mul_f32 v[96:97], v[92:93], v[96:97]
	v_mov_b32_e32 v98, v119
	v_add_f32_e32 v96, v96, v97
	v_add_f32_e32 v96, v102, v96
	v_fma_f32 v96, v106, v96, v110
	v_max_f32_e32 v102, 0, v96
	v_pk_mul_f32 v[96:97], v[92:93], v[98:99]
	s_nop 0
	v_add_f32_e32 v104, v96, v97
	ds_read_b128 v[96:99], v166 offset:64
	v_add_f32_e32 v103, v103, v104
	v_fmac_f32_e32 v111, v107, v103
	v_max_f32_e32 v103, 0, v111
	v_cvt_pk_f16_f32 v103, v102, v103
	v_cvt_pk_f16_f32 v102, v100, v101
	v_cvt_pk_f16_f32 v101, v114, v115
	v_cvt_pk_f16_f32 v100, v95, v120
	ds_read_b128 v[104:107], v166 offset:96
	v_or_b32_e32 v95, 0x1f8c0, v94
	s_waitcnt lgkmcnt(1)
	v_mfma_f32_32x32x16_f16 v[48:63], v[96:99], v[100:103], v[48:63]
	ds_read_b128 v[96:99], v166 offset:8768
	ds_read_b128 v[108:111], v166 offset:8800
	v_or_b32_e32 v120, 0x1fac0, v94
	s_waitcnt lgkmcnt(1)
	v_mfma_f32_32x32x16_f16 v[32:47], v[96:99], v[100:103], v[32:47]
	ds_read_b128 v[96:99], v166 offset:17472
	ds_read_b128 v[112:115], v166 offset:17504
	s_waitcnt lgkmcnt(1)
	v_mfma_f32_32x32x16_f16 v[16:31], v[96:99], v[100:103], v[16:31]
	ds_read_b128 v[96:99], v166 offset:26176
	ds_read_b128 v[116:119], v95
	ds_read_b128 v[120:123], v120
	ds_read_b128 v[168:171], v166 offset:26208
	v_or_b32_e32 v95, 0x1fcc0, v94
	s_waitcnt lgkmcnt(3)
	v_mfma_f32_32x32x16_f16 v[0:15], v[96:99], v[100:103], v[0:15]
	s_waitcnt lgkmcnt(2)
	v_mov_b32_e32 v96, v116
	s_waitcnt lgkmcnt(1)
	v_mov_b32_e32 v97, v120
	v_or_b32_e32 v100, 0x1fec0, v94
	v_pk_mul_f32 v[124:125], v[92:93], v[96:97]
	ds_read_b128 v[96:99], v95
	ds_read_b128 v[100:103], v100
	v_or_b32_e32 v95, 0x200c0, v94
	ds_read_b128 v[172:175], v95
	v_add_f32_e32 v95, v124, v125
	v_mov_b32_e32 v120, v117
	s_waitcnt lgkmcnt(2)
	v_add_f32_e32 v95, v96, v95
	v_or_b32_e32 v96, 0x1f8d0, v94
	v_pk_mul_f32 v[116:117], v[92:93], v[120:121]
	ds_read_b128 v[176:179], v96
	v_add_f32_e32 v96, v116, v117
	v_add_f32_e32 v96, v97, v96
	s_waitcnt lgkmcnt(1)
	v_fma_f32 v96, v101, v96, v173
	v_max_f32_e32 v167, 0, v96
	v_mov_b32_e32 v96, v118
	v_mov_b32_e32 v97, v122
	v_pk_mul_f32 v[96:97], v[92:93], v[96:97]
	v_mov_b32_e32 v122, v119
	v_add_f32_e32 v96, v96, v97
	v_add_f32_e32 v96, v98, v96
	v_fma_f32 v96, v102, v96, v174
	v_fma_f32 v95, v100, v95, v172
	v_max_f32_e32 v172, 0, v96
	v_pk_mul_f32 v[96:97], v[92:93], v[122:123]
	v_or_b32_e32 v100, 0x1fcd0, v94
	v_add_f32_e32 v96, v96, v97
	v_add_f32_e32 v96, v99, v96
	v_fmac_f32_e32 v175, v103, v96
	v_or_b32_e32 v96, 0x1fad0, v94
	ds_read_b128 v[96:99], v96
	ds_read_b128 v[100:103], v100
	v_or_b32_e32 v116, 0x1fed0, v94
	v_or_b32_e32 v120, 0x200d0, v94
	ds_read_b128 v[116:119], v116
	ds_read_b128 v[120:123], v120
	s_waitcnt lgkmcnt(4)
	v_mov_b32_e32 v124, v176
	s_waitcnt lgkmcnt(3)
	v_mov_b32_e32 v125, v96
	v_pk_mul_f32 v[124:125], v[92:93], v[124:125]
	v_max_f32_e32 v95, 0, v95
	v_add_f32_e32 v96, v124, v125
	s_waitcnt lgkmcnt(2)
	v_add_f32_e32 v96, v100, v96
	s_waitcnt lgkmcnt(0)
	v_fma_f32 v96, v116, v96, v120
	v_max_f32_e32 v100, 0, v96
	v_mov_b32_e32 v96, v177
	v_pk_mul_f32 v[96:97], v[92:93], v[96:97]
	v_max_f32_e32 v173, 0, v175
	v_add_f32_e32 v96, v96, v97
	v_add_f32_e32 v96, v101, v96
	v_fma_f32 v96, v117, v96, v121
	v_max_f32_e32 v101, 0, v96
	v_mov_b32_e32 v96, v178
	v_mov_b32_e32 v97, v98
	v_pk_mul_f32 v[96:97], v[92:93], v[96:97]
	v_mov_b32_e32 v98, v179
	v_add_f32_e32 v96, v96, v97
	v_add_f32_e32 v96, v102, v96
	v_fma_f32 v96, v118, v96, v122
	v_max_f32_e32 v102, 0, v96
	v_pk_mul_f32 v[96:97], v[92:93], v[98:99]
	v_cvt_pk_f16_f32 v98, v100, v101
	v_add_f32_e32 v96, v96, v97
	v_add_f32_e32 v96, v103, v96
	v_fmac_f32_e32 v123, v119, v96
	v_max_f32_e32 v96, 0, v123
	v_cvt_pk_f16_f32 v99, v102, v96
	v_cvt_pk_f16_f32 v97, v172, v173
	v_cvt_pk_f16_f32 v96, v95, v167
	v_or_b32_e32 v95, 0x1f900, v94
	s_nop 0
	v_mfma_f32_32x32x16_f16 v[48:63], v[104:107], v[96:99], v[48:63]
	v_or_b32_e32 v104, 0x1fb00, v94
	ds_read_b128 v[100:103], v95
	ds_read_b128 v[104:107], v104
	v_or_b32_e32 v95, 0x1fd00, v94
	v_mfma_f32_32x32x16_f16 v[32:47], v[108:111], v[96:99], v[32:47]
	v_mfma_f32_32x32x16_f16 v[16:31], v[112:115], v[96:99], v[16:31]
	v_mfma_f32_32x32x16_f16 v[0:15], v[168:171], v[96:99], v[0:15]
	s_waitcnt lgkmcnt(1)
	v_mov_b32_e32 v96, v100
	s_waitcnt lgkmcnt(0)
	v_mov_b32_e32 v97, v104
	v_mul_f32_e64 v116, v92, v96
	v_mul_f32_e64 v117, v93, v97
	v_or_b32_e32 v100, 0x1ff00, v94
	ds_read_b128 v[96:99], v95
	ds_read_b128 v[108:111], v100
	v_or_b32_e32 v95, 0x20100, v94
	ds_read_b128 v[112:115], v95
	v_add_f32_e32 v95, v116, v117
	v_mov_b32_e32 v104, v101
	s_waitcnt lgkmcnt(2)
	v_add_f32_e32 v95, v96, v95
	v_or_b32_e32 v96, 0x1f910, v94
	v_pk_mul_f32 v[100:101], v[92:93], v[104:105]
	ds_read_b128 v[116:119], v96
	v_add_f32_e32 v96, v100, v101
	v_add_f32_e32 v96, v97, v96
	s_waitcnt lgkmcnt(1)
	v_fma_f32 v96, v109, v96, v113
	v_max_f32_e32 v120, 0, v96
	v_mov_b32_e32 v96, v102
	v_mov_b32_e32 v97, v106
	v_pk_mul_f32 v[96:97], v[92:93], v[96:97]
	v_mov_b32_e32 v106, v103
	v_add_f32_e32 v96, v96, v97
	v_add_f32_e32 v96, v98, v96
	v_fma_f32 v96, v110, v96, v114
	v_max_f32_e32 v114, 0, v96
	v_pk_mul_f32 v[96:97], v[92:93], v[106:107]
	v_or_b32_e32 v100, 0x1fd10, v94
	v_add_f32_e32 v96, v96, v97
	v_add_f32_e32 v96, v99, v96
	v_fmac_f32_e32 v115, v111, v96
	v_or_b32_e32 v96, 0x1fb10, v94
	ds_read_b128 v[96:99], v96
	ds_read_b128 v[100:103], v100
	v_fma_f32 v95, v108, v95, v112
	v_or_b32_e32 v104, 0x1ff10, v94
	v_or_b32_e32 v108, 0x20110, v94
	ds_read_b128 v[104:107], v104
	ds_read_b128 v[108:111], v108
	s_waitcnt lgkmcnt(4)
	v_mov_b32_e32 v112, v116
	s_waitcnt lgkmcnt(3)
	v_mov_b32_e32 v113, v96
	v_pk_mul_f32 v[112:113], v[92:93], v[112:113]
	v_max_f32_e32 v95, 0, v95
	v_add_f32_e32 v96, v112, v113
	s_waitcnt lgkmcnt(2)
	v_add_f32_e32 v96, v100, v96
	s_waitcnt lgkmcnt(0)
	v_fma_f32 v96, v104, v96, v108
	v_max_f32_e32 v100, 0, v96
	v_mov_b32_e32 v96, v117
	v_pk_mul_f32 v[96:97], v[92:93], v[96:97]
	v_max_f32_e32 v115, 0, v115
	v_add_f32_e32 v96, v96, v97
	v_add_f32_e32 v96, v101, v96
	v_fma_f32 v96, v105, v96, v109
	v_max_f32_e32 v101, 0, v96
	v_mov_b32_e32 v96, v118
	v_mov_b32_e32 v97, v98
	v_pk_mul_f32 v[96:97], v[92:93], v[96:97]
	v_mov_b32_e32 v98, v119
	v_add_f32_e32 v96, v96, v97
	v_add_f32_e32 v96, v102, v96
	v_fma_f32 v96, v106, v96, v110
	v_max_f32_e32 v102, 0, v96
	v_pk_mul_f32 v[96:97], v[92:93], v[98:99]
	s_nop 0
	v_add_f32_e32 v104, v96, v97
	ds_read_b128 v[96:99], v166 offset:128
	v_add_f32_e32 v103, v103, v104
	v_fmac_f32_e32 v111, v107, v103
	v_max_f32_e32 v103, 0, v111
	v_cvt_pk_f16_f32 v103, v102, v103
	v_cvt_pk_f16_f32 v102, v100, v101
	v_cvt_pk_f16_f32 v101, v114, v115
	v_cvt_pk_f16_f32 v100, v95, v120
	ds_read_b128 v[104:107], v166 offset:160
	v_or_b32_e32 v95, 0x1f940, v94
	s_waitcnt lgkmcnt(1)
	v_mfma_f32_32x32x16_f16 v[48:63], v[96:99], v[100:103], v[48:63]
	ds_read_b128 v[96:99], v166 offset:8832
	ds_read_b128 v[108:111], v166 offset:8864
	v_or_b32_e32 v120, 0x1fb40, v94
	s_waitcnt lgkmcnt(1)
	v_mfma_f32_32x32x16_f16 v[32:47], v[96:99], v[100:103], v[32:47]
	ds_read_b128 v[96:99], v166 offset:17536
	ds_read_b128 v[112:115], v166 offset:17568
	s_waitcnt lgkmcnt(1)
	v_mfma_f32_32x32x16_f16 v[16:31], v[96:99], v[100:103], v[16:31]
	ds_read_b128 v[96:99], v166 offset:26240
	ds_read_b128 v[116:119], v95
	ds_read_b128 v[120:123], v120
	ds_read_b128 v[168:171], v166 offset:26272
	v_or_b32_e32 v95, 0x1fd40, v94
	s_waitcnt lgkmcnt(3)
	v_mfma_f32_32x32x16_f16 v[0:15], v[96:99], v[100:103], v[0:15]
	s_waitcnt lgkmcnt(2)
	v_mov_b32_e32 v96, v116
	s_waitcnt lgkmcnt(1)
	v_mov_b32_e32 v97, v120
	v_or_b32_e32 v100, 0x1ff40, v94
	v_pk_mul_f32 v[124:125], v[92:93], v[96:97]
	ds_read_b128 v[96:99], v95
	ds_read_b128 v[100:103], v100
	v_or_b32_e32 v95, 0x20140, v94
	ds_read_b128 v[172:175], v95
	v_add_f32_e32 v95, v124, v125
	v_mov_b32_e32 v120, v117
	s_waitcnt lgkmcnt(2)
	v_add_f32_e32 v95, v96, v95
	v_or_b32_e32 v96, 0x1f950, v94
	v_pk_mul_f32 v[116:117], v[92:93], v[120:121]
	ds_read_b128 v[176:179], v96
	v_add_f32_e32 v96, v116, v117
	v_add_f32_e32 v96, v97, v96
	s_waitcnt lgkmcnt(1)
	v_fma_f32 v96, v101, v96, v173
	v_max_f32_e32 v167, 0, v96
	v_mov_b32_e32 v96, v118
	v_mov_b32_e32 v97, v122
	v_pk_mul_f32 v[96:97], v[92:93], v[96:97]
	v_mov_b32_e32 v122, v119
	v_add_f32_e32 v96, v96, v97
	v_add_f32_e32 v96, v98, v96
	v_fma_f32 v96, v102, v96, v174
	v_fma_f32 v95, v100, v95, v172
	v_max_f32_e32 v172, 0, v96
	v_pk_mul_f32 v[96:97], v[92:93], v[122:123]
	v_or_b32_e32 v100, 0x1fd50, v94
	v_add_f32_e32 v96, v96, v97
	v_add_f32_e32 v96, v99, v96
	v_fmac_f32_e32 v175, v103, v96
	v_or_b32_e32 v96, 0x1fb50, v94
	ds_read_b128 v[96:99], v96
	ds_read_b128 v[100:103], v100
	v_or_b32_e32 v116, 0x1ff50, v94
	v_or_b32_e32 v120, 0x20150, v94
	ds_read_b128 v[116:119], v116
	ds_read_b128 v[120:123], v120
	s_waitcnt lgkmcnt(4)
	v_mov_b32_e32 v124, v176
	s_waitcnt lgkmcnt(3)
	v_mov_b32_e32 v125, v96
	v_pk_mul_f32 v[124:125], v[92:93], v[124:125]
	v_max_f32_e32 v95, 0, v95
	v_add_f32_e32 v96, v124, v125
	s_waitcnt lgkmcnt(2)
	v_add_f32_e32 v96, v100, v96
	s_waitcnt lgkmcnt(0)
	v_fma_f32 v96, v116, v96, v120
	v_max_f32_e32 v100, 0, v96
	v_mov_b32_e32 v96, v177
	v_pk_mul_f32 v[96:97], v[92:93], v[96:97]
	v_max_f32_e32 v173, 0, v175
	v_add_f32_e32 v96, v96, v97
	v_add_f32_e32 v96, v101, v96
	v_fma_f32 v96, v117, v96, v121
	v_max_f32_e32 v101, 0, v96
	v_mov_b32_e32 v96, v178
	v_mov_b32_e32 v97, v98
	v_pk_mul_f32 v[96:97], v[92:93], v[96:97]
	v_mov_b32_e32 v98, v179
	v_add_f32_e32 v96, v96, v97
	v_add_f32_e32 v96, v102, v96
	v_fma_f32 v96, v118, v96, v122
	v_max_f32_e32 v102, 0, v96
	v_pk_mul_f32 v[96:97], v[92:93], v[98:99]
	v_cvt_pk_f16_f32 v98, v100, v101
	v_add_f32_e32 v96, v96, v97
	v_add_f32_e32 v96, v103, v96
	v_fmac_f32_e32 v123, v119, v96
	v_max_f32_e32 v96, 0, v123
	v_cvt_pk_f16_f32 v99, v102, v96
	v_cvt_pk_f16_f32 v97, v172, v173
	v_cvt_pk_f16_f32 v96, v95, v167
	v_or_b32_e32 v95, 0x1f980, v94
	s_nop 0
	v_mfma_f32_32x32x16_f16 v[48:63], v[104:107], v[96:99], v[48:63]
	v_or_b32_e32 v104, 0x1fb80, v94
	ds_read_b128 v[100:103], v95
	ds_read_b128 v[104:107], v104
	v_or_b32_e32 v95, 0x1fd80, v94
	v_mfma_f32_32x32x16_f16 v[32:47], v[108:111], v[96:99], v[32:47]
	v_mfma_f32_32x32x16_f16 v[16:31], v[112:115], v[96:99], v[16:31]
	v_mfma_f32_32x32x16_f16 v[0:15], v[168:171], v[96:99], v[0:15]
	s_waitcnt lgkmcnt(1)
	v_mov_b32_e32 v96, v100
	s_waitcnt lgkmcnt(0)
	v_mov_b32_e32 v97, v104
	v_mul_f32_e64 v116, v92, v96
	v_mul_f32_e64 v117, v93, v97
	v_or_b32_e32 v100, 0x1ff80, v94
	ds_read_b128 v[96:99], v95
	ds_read_b128 v[108:111], v100
	v_or_b32_e32 v95, 0x20180, v94
	ds_read_b128 v[112:115], v95
	v_add_f32_e32 v95, v116, v117
	v_mov_b32_e32 v104, v101
	s_waitcnt lgkmcnt(2)
	v_add_f32_e32 v95, v96, v95
	v_or_b32_e32 v96, 0x1f990, v94
	v_pk_mul_f32 v[100:101], v[92:93], v[104:105]
	ds_read_b128 v[116:119], v96
	v_add_f32_e32 v96, v100, v101
	v_add_f32_e32 v96, v97, v96
	s_waitcnt lgkmcnt(1)
	v_fma_f32 v96, v109, v96, v113
	v_max_f32_e32 v120, 0, v96
	v_mov_b32_e32 v96, v102
	v_mov_b32_e32 v97, v106
	v_pk_mul_f32 v[96:97], v[92:93], v[96:97]
	v_mov_b32_e32 v106, v103
	v_add_f32_e32 v96, v96, v97
	v_add_f32_e32 v96, v98, v96
	v_fma_f32 v96, v110, v96, v114
	v_max_f32_e32 v114, 0, v96
	v_pk_mul_f32 v[96:97], v[92:93], v[106:107]
	v_or_b32_e32 v100, 0x1fd90, v94
	v_add_f32_e32 v96, v96, v97
	v_add_f32_e32 v96, v99, v96
	v_fmac_f32_e32 v115, v111, v96
	v_or_b32_e32 v96, 0x1fb90, v94
	ds_read_b128 v[96:99], v96
	ds_read_b128 v[100:103], v100
	v_fma_f32 v95, v108, v95, v112
	v_or_b32_e32 v104, 0x1ff90, v94
	v_or_b32_e32 v108, 0x20190, v94
	ds_read_b128 v[104:107], v104
	ds_read_b128 v[108:111], v108
	s_waitcnt lgkmcnt(4)
	v_mov_b32_e32 v112, v116
	s_waitcnt lgkmcnt(3)
	v_mov_b32_e32 v113, v96
	v_pk_mul_f32 v[112:113], v[92:93], v[112:113]
	v_max_f32_e32 v95, 0, v95
	v_add_f32_e32 v96, v112, v113
	s_waitcnt lgkmcnt(2)
	v_add_f32_e32 v96, v100, v96
	s_waitcnt lgkmcnt(0)
	v_fma_f32 v96, v104, v96, v108
	v_max_f32_e32 v100, 0, v96
	v_mov_b32_e32 v96, v117
	v_pk_mul_f32 v[96:97], v[92:93], v[96:97]
	v_max_f32_e32 v115, 0, v115
	v_add_f32_e32 v96, v96, v97
	v_add_f32_e32 v96, v101, v96
	v_fma_f32 v96, v105, v96, v109
	v_max_f32_e32 v101, 0, v96
	v_mov_b32_e32 v96, v118
	v_mov_b32_e32 v97, v98
	v_pk_mul_f32 v[96:97], v[92:93], v[96:97]
	v_mov_b32_e32 v98, v119
	v_add_f32_e32 v96, v96, v97
	v_add_f32_e32 v96, v102, v96
	v_fma_f32 v96, v106, v96, v110
	v_max_f32_e32 v102, 0, v96
	v_pk_mul_f32 v[96:97], v[92:93], v[98:99]
	s_nop 0
	v_add_f32_e32 v104, v96, v97
	ds_read_b128 v[96:99], v166 offset:192
	v_add_f32_e32 v103, v103, v104
	v_fmac_f32_e32 v111, v107, v103
	v_max_f32_e32 v103, 0, v111
	v_cvt_pk_f16_f32 v103, v102, v103
	v_cvt_pk_f16_f32 v102, v100, v101
	v_cvt_pk_f16_f32 v101, v114, v115
	v_cvt_pk_f16_f32 v100, v95, v120
	ds_read_b128 v[104:107], v166 offset:224
	v_or_b32_e32 v95, 0x1f9c0, v94
	s_waitcnt lgkmcnt(1)
	v_mfma_f32_32x32x16_f16 v[48:63], v[96:99], v[100:103], v[48:63]
	ds_read_b128 v[96:99], v166 offset:8896
	ds_read_b128 v[108:111], v166 offset:8928
	v_or_b32_e32 v120, 0x1fbc0, v94
	s_waitcnt lgkmcnt(1)
	v_mfma_f32_32x32x16_f16 v[32:47], v[96:99], v[100:103], v[32:47]
	ds_read_b128 v[96:99], v166 offset:17600
	ds_read_b128 v[112:115], v166 offset:17632
	s_waitcnt lgkmcnt(1)
	v_mfma_f32_32x32x16_f16 v[16:31], v[96:99], v[100:103], v[16:31]
	ds_read_b128 v[96:99], v166 offset:26304
	ds_read_b128 v[116:119], v95
	ds_read_b128 v[120:123], v120
	ds_read_b128 v[168:171], v166 offset:26336
	v_or_b32_e32 v95, 0x1fdc0, v94
	s_waitcnt lgkmcnt(3)
	v_mfma_f32_32x32x16_f16 v[0:15], v[96:99], v[100:103], v[0:15]
	s_waitcnt lgkmcnt(2)
	v_mov_b32_e32 v96, v116
	s_waitcnt lgkmcnt(1)
	v_mov_b32_e32 v97, v120
	v_or_b32_e32 v100, 0x1ffc0, v94
	v_pk_mul_f32 v[124:125], v[92:93], v[96:97]
	ds_read_b128 v[96:99], v95
	ds_read_b128 v[100:103], v100
	v_or_b32_e32 v95, 0x201c0, v94
	ds_read_b128 v[172:175], v95
	v_add_f32_e32 v95, v124, v125
	s_waitcnt lgkmcnt(2)
	v_add_f32_e32 v95, v96, v95
	v_mov_b32_e32 v120, v117
	v_pk_mul_f32 v[116:117], v[92:93], v[120:121]
	s_waitcnt lgkmcnt(0)
	v_fma_f32 v95, v100, v95, v172
	v_or_b32_e32 v96, 0x1f9d0, v94
	v_max_f32_e32 v167, 0, v95
	v_add_f32_e32 v95, v116, v117
	ds_read_b128 v[176:179], v96
	v_add_f32_e32 v95, v97, v95
	v_mov_b32_e32 v96, v118
	v_mov_b32_e32 v97, v122
	v_fma_f32 v95, v101, v95, v173
	v_pk_mul_f32 v[96:97], v[92:93], v[96:97]
	v_max_f32_e32 v172, 0, v95
	v_add_f32_e32 v95, v96, v97
	v_add_f32_e32 v95, v98, v95
	v_mov_b32_e32 v122, v119
	v_fma_f32 v95, v102, v95, v174
	v_pk_mul_f32 v[96:97], v[92:93], v[122:123]
	v_max_f32_e32 v173, 0, v95
	v_add_f32_e32 v95, v96, v97
	v_add_f32_e32 v95, v99, v95
	v_fmac_f32_e32 v175, v103, v95
	v_or_b32_e32 v95, 0x1fbd0, v94
	v_or_b32_e32 v100, 0x1fdd0, v94
	ds_read_b128 v[96:99], v95
	ds_read_b128 v[100:103], v100
	v_or_b32_e32 v95, 0x1ffd0, v94
	v_or_b32_e32 v94, 0x201d0, v94
	ds_read_b128 v[116:119], v95
	ds_read_b128 v[120:123], v94
	s_waitcnt lgkmcnt(4)
	v_mov_b32_e32 v124, v176
	s_waitcnt lgkmcnt(3)
	v_mov_b32_e32 v125, v96
	v_pk_mul_f32 v[94:95], v[92:93], v[124:125]
	v_mov_b32_e32 v96, v177
	v_add_f32_e32 v94, v94, v95
	s_waitcnt lgkmcnt(2)
	v_add_f32_e32 v94, v100, v94
	s_waitcnt lgkmcnt(0)
	v_fma_f32 v94, v116, v94, v120
	v_max_f32_e32 v100, 0, v94
	v_pk_mul_f32 v[94:95], v[92:93], v[96:97]
	v_max_f32_e32 v174, 0, v175
	v_add_f32_e32 v94, v94, v95
	v_add_f32_e32 v94, v101, v94
	v_fma_f32 v94, v117, v94, v121
	v_max_f32_e32 v96, 0, v94
	v_mov_b32_e32 v94, v178
	v_mov_b32_e32 v95, v98
	v_mov_b32_e32 v98, v179
	v_pk_mul_f32 v[94:95], v[92:93], v[94:95]
	v_pk_mul_f32 v[92:93], v[92:93], v[98:99]
	v_add_f32_e32 v94, v94, v95
	v_add_f32_e32 v92, v92, v93
	v_add_f32_e32 v94, v102, v94
	v_add_f32_e32 v92, v103, v92
	v_fma_f32 v94, v118, v94, v122
	v_fmac_f32_e32 v123, v119, v92
	v_max_f32_e32 v94, 0, v94
	v_max_f32_e32 v92, 0, v123
	v_cvt_pk_f16_f32 v95, v94, v92
	v_cvt_pk_f16_f32 v94, v100, v96
	v_cvt_pk_f16_f32 v93, v173, v174
	v_cvt_pk_f16_f32 v92, v167, v172
	s_waitcnt vmcnt(16)
	v_cvt_f32_f16_sdwa v183, v163 dst_sel:DWORD dst_unused:UNUSED_PAD src0_sel:WORD_1
	v_cvt_f32_f16_e32 v182, v163
	v_cvt_f32_f16_sdwa v163, v127 dst_sel:DWORD dst_unused:UNUSED_PAD src0_sel:WORD_1
	v_cvt_f32_f16_sdwa v97, v90 dst_sel:DWORD dst_unused:UNUSED_PAD src0_sel:WORD_1
	v_cvt_f32_f16_e32 v96, v90
	v_mfma_f32_32x32x16_f16 v[48:63], v[104:107], v[92:95], v[48:63]
	v_cvt_f32_f16_sdwa v99, v88 dst_sel:DWORD dst_unused:UNUSED_PAD src0_sel:WORD_1
	v_cvt_f32_f16_e32 v98, v88
	v_or_b32_e32 v88, 0x21600, v165
	v_cvt_f32_f16_sdwa v101, v89 dst_sel:DWORD dst_unused:UNUSED_PAD src0_sel:WORD_1
	v_cvt_f32_f16_e32 v100, v89
	v_pk_fma_f32 v[96:97], v[98:99], s[4:5], v[96:97] op_sel_hi:[1,0,1]
	v_cvt_f32_f16_sdwa v99, v91 dst_sel:DWORD dst_unused:UNUSED_PAD src0_sel:WORD_1
	v_mfma_f32_32x32x16_f16 v[32:47], v[108:111], v[92:95], v[32:47]
	v_cvt_f32_f16_e32 v98, v91
	v_mfma_f32_32x32x16_f16 v[16:31], v[112:115], v[92:95], v[16:31]
	v_mfma_f32_32x32x16_f16 v[0:15], v[168:171], v[92:95], v[0:15]
	ds_read_b128 v[92:95], v88
	v_or_b32_e32 v88, 0x21620, v165
	ds_read_b128 v[88:91], v88
	s_waitcnt lgkmcnt(1)
	v_add_f32_e64 v48, v48, v92
	v_add_f32_e64 v49, v49, v93
	v_pk_add_f32 v[48:49], v[96:97], v[48:49]
	v_cvt_f32_f16_sdwa v93, v86 dst_sel:DWORD dst_unused:UNUSED_PAD src0_sel:WORD_1
	v_cvt_f32_f16_e32 v92, v86
	v_cvt_f32_f16_sdwa v97, v84 dst_sel:DWORD dst_unused:UNUSED_PAD src0_sel:WORD_1
	v_cvt_f32_f16_e32 v96, v84
	v_cvt_pk_f16_f32 v112, v48, v49
	v_pk_fma_f32 v[48:49], v[100:101], s[4:5], v[98:99] op_sel_hi:[1,0,1]
	v_pk_add_f32 v[50:51], v[50:51], v[94:95]
	v_cvt_f32_f16_e32 v86, v85
	v_pk_add_f32 v[48:49], v[48:49], v[50:51]
	v_cvt_f32_f16_sdwa v51, v87 dst_sel:DWORD dst_unused:UNUSED_PAD src0_sel:WORD_1
	v_cvt_f32_f16_e32 v50, v87
	v_cvt_f32_f16_sdwa v87, v85 dst_sel:DWORD dst_unused:UNUSED_PAD src0_sel:WORD_1
	v_cvt_pk_f16_f32 v113, v48, v49
	v_pk_fma_f32 v[48:49], v[96:97], s[4:5], v[92:93] op_sel_hi:[1,0,1]
	s_waitcnt lgkmcnt(0)
	v_pk_add_f32 v[52:53], v[52:53], v[88:89]
	s_nop 0
	v_pk_add_f32 v[48:49], v[48:49], v[52:53]
	v_cvt_f32_f16_sdwa v53, v82 dst_sel:DWORD dst_unused:UNUSED_PAD src0_sel:WORD_1
	v_cvt_pk_f16_f32 v114, v48, v49
	v_pk_fma_f32 v[48:49], v[86:87], s[4:5], v[50:51] op_sel_hi:[1,0,1]
	v_pk_add_f32 v[50:51], v[54:55], v[90:91]
	v_cvt_f32_f16_e32 v52, v82
	v_pk_add_f32 v[48:49], v[48:49], v[50:51]
	v_cvt_f32_f16_sdwa v55, v80 dst_sel:DWORD dst_unused:UNUSED_PAD src0_sel:WORD_1
	v_cvt_pk_f16_f32 v115, v48, v49
	v_or_b32_e32 v48, 0x21640, v165
	v_cvt_f32_f16_e32 v54, v80
	ds_read_b128 v[48:51], v48
	v_cvt_f32_f16_sdwa v87, v83 dst_sel:DWORD dst_unused:UNUSED_PAD src0_sel:WORD_1
	v_cvt_f32_f16_e32 v86, v83
	v_cvt_f32_f16_sdwa v83, v81 dst_sel:DWORD dst_unused:UNUSED_PAD src0_sel:WORD_1
	v_cvt_f32_f16_e32 v82, v81
	v_pk_fma_f32 v[84:85], v[54:55], s[4:5], v[52:53] op_sel_hi:[1,0,1]
	v_or_b32_e32 v52, 0x21660, v165
	ds_read_b128 v[52:55], v52
	s_waitcnt lgkmcnt(1)
	v_pk_add_f32 v[48:49], v[56:57], v[48:49]
	v_cvt_f32_f16_sdwa v57, v78 dst_sel:DWORD dst_unused:UNUSED_PAD src0_sel:WORD_1
	v_cvt_f32_f16_e32 v56, v78
	v_cvt_f32_f16_sdwa v81, v76 dst_sel:DWORD dst_unused:UNUSED_PAD src0_sel:WORD_1
	v_cvt_f32_f16_e32 v80, v76
	v_pk_add_f32 v[48:49], v[84:85], v[48:49]
	v_pk_add_f32 v[50:51], v[58:59], v[50:51]
	v_cvt_pk_f16_f32 v116, v48, v49
	v_pk_fma_f32 v[48:49], v[82:83], s[4:5], v[86:87] op_sel_hi:[1,0,1]
	s_waitcnt lgkmcnt(0)
	v_pk_add_f32 v[52:53], v[60:61], v[52:53]
	v_pk_add_f32 v[48:49], v[48:49], v[50:51]
	v_cvt_f32_f16_sdwa v51, v79 dst_sel:DWORD dst_unused:UNUSED_PAD src0_sel:WORD_1
	v_cvt_pk_f16_f32 v117, v48, v49
	v_pk_fma_f32 v[48:49], v[80:81], s[4:5], v[56:57] op_sel_hi:[1,0,1]
	v_cvt_f32_f16_e32 v50, v79
	v_cvt_f32_f16_sdwa v57, v77 dst_sel:DWORD dst_unused:UNUSED_PAD src0_sel:WORD_1
	v_cvt_f32_f16_e32 v56, v77
	v_pk_add_f32 v[48:49], v[48:49], v[52:53]
	v_cvt_f32_f16_sdwa v53, v74 dst_sel:DWORD dst_unused:UNUSED_PAD src0_sel:WORD_1
	v_cvt_pk_f16_f32 v118, v48, v49
	v_pk_fma_f32 v[48:49], v[56:57], s[4:5], v[50:51] op_sel_hi:[1,0,1]
	v_pk_add_f32 v[50:51], v[62:63], v[54:55]
	v_cvt_f32_f16_e32 v52, v74
	v_pk_add_f32 v[48:49], v[48:49], v[50:51]
	v_cvt_f32_f16_sdwa v55, v72 dst_sel:DWORD dst_unused:UNUSED_PAD src0_sel:WORD_1
	v_cvt_pk_f16_f32 v119, v48, v49
	v_or_b32_e32 v48, 0x21680, v165
	v_cvt_f32_f16_e32 v54, v72
	ds_read_b128 v[48:51], v48
	v_cvt_f32_f16_sdwa v59, v75 dst_sel:DWORD dst_unused:UNUSED_PAD src0_sel:WORD_1
	v_cvt_f32_f16_e32 v58, v75
	v_pk_fma_f32 v[56:57], v[54:55], s[4:5], v[52:53] op_sel_hi:[1,0,1]
	v_cvt_f32_f16_sdwa v61, v73 dst_sel:DWORD dst_unused:UNUSED_PAD src0_sel:WORD_1
	v_cvt_f32_f16_e32 v60, v73
	v_or_b32_e32 v52, 0x216a0, v165
	ds_read_b128 v[52:55], v52
	s_waitcnt lgkmcnt(1)
	v_pk_add_f32 v[32:33], v[32:33], v[48:49]
	v_cvt_f32_f16_sdwa v49, v70 dst_sel:DWORD dst_unused:UNUSED_PAD src0_sel:WORD_1
	v_pk_add_f32 v[32:33], v[56:57], v[32:33]
	v_cvt_f32_f16_e32 v48, v70
	v_cvt_f32_f16_sdwa v57, v68 dst_sel:DWORD dst_unused:UNUSED_PAD src0_sel:WORD_1
	v_cvt_f32_f16_e32 v56, v68
	v_cvt_pk_f16_f32 v120, v32, v33
	v_pk_fma_f32 v[32:33], v[60:61], s[4:5], v[58:59] op_sel_hi:[1,0,1]
	v_pk_add_f32 v[34:35], v[34:35], v[50:51]
	s_waitcnt lgkmcnt(0)
	v_pk_add_f32 v[36:37], v[36:37], v[52:53]
	v_pk_add_f32 v[32:33], v[32:33], v[34:35]
	v_cvt_f32_f16_sdwa v35, v71 dst_sel:DWORD dst_unused:UNUSED_PAD src0_sel:WORD_1
	v_cvt_pk_f16_f32 v121, v32, v33
	v_pk_fma_f32 v[32:33], v[56:57], s[4:5], v[48:49] op_sel_hi:[1,0,1]
	v_cvt_f32_f16_e32 v34, v71
	v_cvt_f32_f16_sdwa v49, v69 dst_sel:DWORD dst_unused:UNUSED_PAD src0_sel:WORD_1
	v_cvt_f32_f16_e32 v48, v69
	v_pk_add_f32 v[32:33], v[32:33], v[36:37]
	v_cvt_f32_f16_sdwa v37, v66 dst_sel:DWORD dst_unused:UNUSED_PAD src0_sel:WORD_1
	v_cvt_pk_f16_f32 v122, v32, v33
	v_pk_fma_f32 v[32:33], v[48:49], s[4:5], v[34:35] op_sel_hi:[1,0,1]
	v_pk_add_f32 v[34:35], v[38:39], v[54:55]
	v_cvt_f32_f16_e32 v36, v66
	v_cvt_f32_f16_sdwa v39, v64 dst_sel:DWORD dst_unused:UNUSED_PAD src0_sel:WORD_1
	v_cvt_f32_f16_e32 v38, v64
	v_pk_add_f32 v[32:33], v[32:33], v[34:35]
	v_or_b32_e32 v48, 0x216c0, v165
	v_cvt_pk_f16_f32 v123, v32, v33
	v_pk_fma_f32 v[32:33], v[38:39], s[4:5], v[36:37] op_sel_hi:[1,0,1]
	ds_read_b128 v[36:39], v166 offset:34816
	v_cvt_f32_f16_sdwa v35, v67 dst_sel:DWORD dst_unused:UNUSED_PAD src0_sel:WORD_1
	v_cvt_f32_f16_e32 v34, v67
	v_cvt_f32_f16_sdwa v57, v65 dst_sel:DWORD dst_unused:UNUSED_PAD src0_sel:WORD_1
	v_cvt_f32_f16_e32 v56, v65
	v_or_b32_e32 v52, 0x216e0, v165
	ds_read_b128 v[48:51], v48
	ds_read_b128 v[168:171], v52
	ds_read_b128 v[52:55], v166 offset:43520
	ds_read_b128 v[172:175], v166 offset:34848
	s_waitcnt lgkmcnt(4)
	v_mfma_f32_32x32x16_f16 v[96:111], v[36:39], v[112:115], 0
	s_waitcnt lgkmcnt(3)
	v_add_f32_e64 v36, v40, v48
	v_add_f32_e64 v37, v41, v49
	v_fma_f32 v40, v56, s4, v34
	v_fma_f32 v41, v57, s4, v35
	v_pk_add_f32 v[32:33], v[32:33], v[36:37]
	v_pk_add_f32 v[42:43], v[42:43], v[50:51]
	v_cvt_pk_f16_f32 v124, v32, v33
	ds_read_b128 v[32:35], v166 offset:52224
	ds_read_b128 v[36:39], v166 offset:43552
	v_pk_add_f32 v[48:49], v[40:41], v[42:43]
	s_waitcnt lgkmcnt(3)
	v_mfma_f32_32x32x16_f16 v[80:95], v[52:55], v[112:115], 0
	v_cvt_f32_f16_sdwa v51, v162 dst_sel:DWORD dst_unused:UNUSED_PAD src0_sel:WORD_1
	v_cvt_f32_f16_e32 v50, v162
	v_cvt_f32_f16_sdwa v53, v126 dst_sel:DWORD dst_unused:UNUSED_PAD src0_sel:WORD_1
	v_cvt_f32_f16_e32 v52, v126
	ds_read_b128 v[40:43], v166 offset:60928
	ds_read_b128 v[176:179], v166 offset:52256
	v_cvt_f32_f16_e32 v162, v127
	v_cvt_pk_f16_f32 v125, v48, v49
	v_pk_fma_f32 v[180:181], v[52:53], s[4:5], v[50:51] op_sel_hi:[1,0,1]
	s_waitcnt lgkmcnt(1)
	v_mfma_f32_32x32x16_f16 v[48:63], v[40:43], v[112:115], 0
	v_add_f32_e64 v40, v44, v168
	v_add_f32_e64 v41, v45, v169
	v_add_f32_e64 v42, v46, v170
	v_add_f32_e64 v43, v47, v171
	v_add_f32_e64 v40, v180, v40
	v_add_f32_e64 v41, v181, v41
	s_waitcnt vmcnt(15)
	v_cvt_f32_f16_sdwa v45, v160 dst_sel:DWORD dst_unused:UNUSED_PAD src0_sel:WORD_1
	v_cvt_pk_f16_f32 v126, v40, v41
	v_pk_fma_f32 v[40:41], v[162:163], s[4:5], v[182:183] op_sel_hi:[1,0,1]
	v_cvt_f32_f16_e32 v44, v160
	v_pk_add_f32 v[40:41], v[40:41], v[42:43]
	s_waitcnt vmcnt(14)
	v_cvt_f32_f16_sdwa v47, v128 dst_sel:DWORD dst_unused:UNUSED_PAD src0_sel:WORD_1
	v_cvt_pk_f16_f32 v127, v40, v41
	v_or_b32_e32 v40, 0x21700, v165
	ds_read_b128 v[40:43], v40
	v_cvt_f32_f16_e32 v46, v128
	v_mfma_f32_32x32x16_f16 v[64:79], v[32:35], v[112:115], 0
	ds_read_b128 v[32:35], v166 offset:60960
	s_waitcnt vmcnt(13)
	v_cvt_f32_f16_e32 v160, v130
	v_fma_f32 v44, v46, s4, v44
	v_fma_f32 v45, v47, s4, v45
	v_cvt_f32_f16_sdwa v47, v129 dst_sel:DWORD dst_unused:UNUSED_PAD src0_sel:WORD_1
	v_cvt_f32_f16_e32 v46, v129
	v_mfma_f32_32x32x16_f16 v[80:95], v[36:39], v[116:119], v[80:95]
	v_or_b32_e32 v36, 0x21720, v165
	ds_read_b128 v[36:39], v36
	s_waitcnt lgkmcnt(2)
	v_add_f32_e64 v16, v16, v40
	v_add_f32_e64 v17, v17, v41
	v_cvt_f32_f16_sdwa v41, v161 dst_sel:DWORD dst_unused:UNUSED_PAD src0_sel:WORD_1
	v_cvt_f32_f16_e32 v40, v161
	v_pk_add_f32 v[16:17], v[44:45], v[16:17]
	v_pk_add_f32 v[18:19], v[18:19], v[42:43]
	v_cvt_pk_f16_f32 v128, v16, v17
	v_pk_fma_f32 v[16:17], v[46:47], s[4:5], v[40:41] op_sel_hi:[1,0,1]
	ds_read_b128 v[44:47], v166 offset:34880
	v_mfma_f32_32x32x16_f16 v[96:111], v[172:175], v[116:119], v[96:111]
	s_waitcnt vmcnt(12)
	v_cvt_f32_f16_sdwa v41, v158 dst_sel:DWORD dst_unused:UNUSED_PAD src0_sel:WORD_1
	v_cvt_f32_f16_e32 v40, v158
	v_cvt_f32_f16_sdwa v161, v130 dst_sel:DWORD dst_unused:UNUSED_PAD src0_sel:WORD_1
	v_add_f32_e64 v16, v16, v18
	v_add_f32_e64 v17, v17, v19
	s_waitcnt lgkmcnt(1)
	v_pk_add_f32 v[20:21], v[20:21], v[36:37]
	v_cvt_pk_f16_f32 v129, v16, v17
	v_cvt_f32_f16_sdwa v37, v159 dst_sel:DWORD dst_unused:UNUSED_PAD src0_sel:WORD_1
	v_mfma_f32_32x32x16_f16 v[48:63], v[32:35], v[116:119], v[48:63]
	ds_read_b128 v[16:19], v166 offset:43584
	ds_read_b128 v[32:35], v166 offset:34912
	v_cvt_f32_f16_e32 v36, v159
	v_cvt_f32_f16_sdwa v159, v131 dst_sel:DWORD dst_unused:UNUSED_PAD src0_sel:WORD_1
	v_cvt_f32_f16_e32 v158, v131
	v_pk_fma_f32 v[160:161], v[160:161], s[4:5], v[40:41] op_sel_hi:[1,0,1]
	v_mfma_f32_32x32x16_f16 v[64:79], v[176:179], v[116:119], v[64:79]
	s_waitcnt lgkmcnt(1)
	v_mfma_f32_32x32x16_f16 v[80:95], v[16:19], v[120:123], v[80:95]
	v_add_f32_e64 v16, v160, v20
	v_add_f32_e64 v17, v161, v21
	v_add_f32_e64 v18, v22, v38
	v_add_f32_e64 v19, v23, v39
	v_cvt_pk_f16_f32 v130, v16, v17
	v_pk_fma_f32 v[16:17], v[158:159], s[4:5], v[36:37] op_sel_hi:[1,0,1]
	s_nop 0
	v_pk_add_f32 v[36:37], v[16:17], v[18:19]
	v_mfma_f32_32x32x16_f16 v[96:111], v[44:47], v[120:123], v[96:111]
	ds_read_b128 v[40:43], v166 offset:52288
	ds_read_b128 v[44:47], v166 offset:43616
	ds_read_b128 v[16:19], v166 offset:60992
	ds_read_b128 v[20:23], v166 offset:52320
	v_cvt_pk_f16_f32 v131, v36, v37
	ds_read_b128 v[36:39], v166 offset:61024
	s_waitcnt lgkmcnt(4)
	v_mfma_f32_32x32x16_f16 v[64:79], v[40:43], v[120:123], v[64:79]
	s_waitcnt vmcnt(10)
	v_cvt_f32_f16_sdwa v43, v132 dst_sel:DWORD dst_unused:UNUSED_PAD src0_sel:WORD_1
	v_cvt_f32_f16_e32 v42, v132
	v_or_b32_e32 v132, 0x21740, v165
	v_cvt_f32_f16_sdwa v41, v156 dst_sel:DWORD dst_unused:UNUSED_PAD src0_sel:WORD_1
	v_cvt_f32_f16_e32 v40, v156
	v_cvt_f32_f16_e32 v156, v133
	v_pk_fma_f32 v[40:41], v[42:43], s[4:5], v[40:41] op_sel_hi:[1,0,1]
	s_waitcnt lgkmcnt(2)
	v_mfma_f32_32x32x16_f16 v[48:63], v[16:19], v[120:123], v[48:63]
	ds_read_b128 v[16:19], v132
	v_cvt_f32_f16_sdwa v43, v157 dst_sel:DWORD dst_unused:UNUSED_PAD src0_sel:WORD_1
	v_cvt_f32_f16_e32 v42, v157
	v_cvt_f32_f16_sdwa v157, v133 dst_sel:DWORD dst_unused:UNUSED_PAD src0_sel:WORD_1
	v_or_b32_e32 v132, 0x21760, v165
	s_waitcnt lgkmcnt(0)
	v_pk_add_f32 v[16:17], v[24:25], v[16:17]
	s_waitcnt vmcnt(8)
	v_cvt_f32_f16_sdwa v25, v154 dst_sel:DWORD dst_unused:UNUSED_PAD src0_sel:WORD_1
	v_mfma_f32_32x32x16_f16 v[96:111], v[32:35], v[124:127], v[96:111]
	ds_read_b128 v[32:35], v132
	v_add_f32_e64 v16, v40, v16
	v_add_f32_e64 v17, v41, v17
	v_cvt_f32_f16_e32 v24, v154
	v_cvt_f32_f16_sdwa v41, v134 dst_sel:DWORD dst_unused:UNUSED_PAD src0_sel:WORD_1
	v_cvt_f32_f16_e32 v40, v134
	v_cvt_pk_f16_f32 v132, v16, v17
	v_pk_fma_f32 v[16:17], v[156:157], s[4:5], v[42:43] op_sel_hi:[1,0,1]
	v_pk_add_f32 v[18:19], v[26:27], v[18:19]
	v_mfma_f32_32x32x16_f16 v[80:95], v[44:47], v[124:127], v[80:95]
	v_add_f32_e64 v16, v16, v18
	v_add_f32_e64 v17, v17, v19
	s_waitcnt lgkmcnt(0)
	v_add_f32_e64 v18, v28, v32
	v_add_f32_e64 v19, v29, v33
	v_cvt_pk_f16_f32 v133, v16, v17
	v_pk_fma_f32 v[16:17], v[40:41], s[4:5], v[24:25] op_sel_hi:[1,0,1]
	v_pk_add_f32 v[30:31], v[30:31], v[34:35]
	v_pk_add_f32 v[16:17], v[16:17], v[18:19]
	s_waitcnt vmcnt(7)
	v_cvt_f32_f16_sdwa v33, v152 dst_sel:DWORD dst_unused:UNUSED_PAD src0_sel:WORD_1
	v_cvt_pk_f16_f32 v134, v16, v17
	ds_read_b128 v[16:19], v166 offset:34944
	v_mfma_f32_32x32x16_f16 v[64:79], v[20:23], v[124:127], v[64:79]
	v_cvt_f32_f16_sdwa v21, v155 dst_sel:DWORD dst_unused:UNUSED_PAD src0_sel:WORD_1
	v_cvt_f32_f16_e32 v20, v155
	v_cvt_f32_f16_sdwa v23, v135 dst_sel:DWORD dst_unused:UNUSED_PAD src0_sel:WORD_1
	v_cvt_f32_f16_e32 v22, v135
	v_cvt_f32_f16_e32 v32, v152
	s_waitcnt vmcnt(6)
	v_cvt_f32_f16_sdwa v35, v136 dst_sel:DWORD dst_unused:UNUSED_PAD src0_sel:WORD_1
	v_cvt_f32_f16_e32 v34, v136
	v_pk_fma_f32 v[28:29], v[22:23], s[4:5], v[20:21] op_sel_hi:[1,0,1]
	ds_read_b128 v[20:23], v166 offset:43648
	ds_read_b128 v[24:27], v166 offset:34976
	s_waitcnt lgkmcnt(2)
	v_mfma_f32_32x32x16_f16 v[96:111], v[16:19], v[128:131], v[96:111]
	v_add_f32_e64 v16, v28, v30
	v_add_f32_e64 v17, v29, v31
	v_fma_f32 v40, v34, s4, v32
	v_fma_f32 v41, v35, s4, v33
	v_cvt_pk_f16_f32 v135, v16, v17
	ds_read_b128 v[16:19], v166 offset:52352
	ds_read_b128 v[28:31], v166 offset:43680
	v_cvt_f32_f16_sdwa v43, v153 dst_sel:DWORD dst_unused:UNUSED_PAD src0_sel:WORD_1
	v_cvt_f32_f16_e32 v42, v153
	v_cvt_f32_f16_sdwa v45, v137 dst_sel:DWORD dst_unused:UNUSED_PAD src0_sel:WORD_1
	v_mfma_f32_32x32x16_f16 v[48:63], v[36:39], v[124:127], v[48:63]
	v_or_b32_e32 v36, 0x21780, v165
	v_cvt_f32_f16_e32 v44, v137
	s_waitcnt lgkmcnt(3)
	v_mfma_f32_32x32x16_f16 v[80:95], v[20:23], v[128:131], v[80:95]
	ds_read_b128 v[20:23], v36
	ds_read_b128 v[32:35], v166 offset:61056
	ds_read_b128 v[36:39], v166 offset:52384
	s_waitcnt lgkmcnt(2)
	v_add_f32_e64 v0, v0, v20
	v_add_f32_e64 v1, v1, v21
	v_pk_add_f32 v[0:1], v[40:41], v[0:1]
	v_mfma_f32_32x32x16_f16 v[64:79], v[16:19], v[128:131], v[64:79]
	v_or_b32_e32 v16, 0x217a0, v165
	ds_read_b128 v[16:19], v16
	v_add_f32_e64 v2, v2, v22
	v_add_f32_e64 v3, v3, v23
	s_waitcnt vmcnt(4)
	v_cvt_f32_f16_sdwa v21, v150 dst_sel:DWORD dst_unused:UNUSED_PAD src0_sel:WORD_1
	v_cvt_f32_f16_e32 v20, v150
	v_cvt_f32_f16_sdwa v23, v138 dst_sel:DWORD dst_unused:UNUSED_PAD src0_sel:WORD_1
	v_cvt_f32_f16_e32 v22, v138
	v_cvt_pk_f16_f32 v136, v0, v1
	v_pk_fma_f32 v[0:1], v[44:45], s[4:5], v[42:43] op_sel_hi:[1,0,1]
	ds_read_b128 v[40:43], v166 offset:61088
	v_pk_add_f32 v[0:1], v[0:1], v[2:3]
	s_waitcnt lgkmcnt(1)
	v_pk_add_f32 v[2:3], v[4:5], v[16:17]
	v_cvt_f32_f16_sdwa v5, v151 dst_sel:DWORD dst_unused:UNUSED_PAD src0_sel:WORD_1
	v_cvt_f32_f16_e32 v4, v151
	v_cvt_f32_f16_sdwa v17, v139 dst_sel:DWORD dst_unused:UNUSED_PAD src0_sel:WORD_1
	v_cvt_f32_f16_e32 v16, v139
	v_cvt_pk_f16_f32 v137, v0, v1
	v_pk_fma_f32 v[0:1], v[22:23], s[4:5], v[20:21] op_sel_hi:[1,0,1]
	v_mfma_f32_32x32x16_f16 v[48:63], v[32:35], v[128:131], v[48:63]
	v_add_f32_e64 v0, v0, v2
	v_add_f32_e64 v1, v1, v3
	v_add_f32_e64 v2, v6, v18
	v_add_f32_e64 v3, v7, v19
	v_cvt_pk_f16_f32 v138, v0, v1
	v_pk_fma_f32 v[0:1], v[16:17], s[4:5], v[4:5] op_sel_hi:[1,0,1]
	s_waitcnt vmcnt(3)
	v_cvt_f32_f16_sdwa v5, v148 dst_sel:DWORD dst_unused:UNUSED_PAD src0_sel:WORD_1
	v_pk_add_f32 v[0:1], v[0:1], v[2:3]
	v_cvt_f32_f16_e32 v4, v148
	v_cvt_pk_f16_f32 v139, v0, v1
	ds_read_b128 v[0:3], v166 offset:35008
	v_mfma_f32_32x32x16_f16 v[96:111], v[24:27], v[132:135], v[96:111]
	s_waitcnt vmcnt(2)
	v_cvt_f32_f16_sdwa v7, v140 dst_sel:DWORD dst_unused:UNUSED_PAD src0_sel:WORD_1
	v_cvt_f32_f16_e32 v6, v140
	v_or_b32_e32 v16, 0x217c0, v165
	v_or_b32_e32 v17, 0x217e0, v165
	v_cvt_f32_f16_sdwa v33, v141 dst_sel:DWORD dst_unused:UNUSED_PAD src0_sel:WORD_1
	v_cvt_f32_f16_e32 v32, v141
	v_mfma_f32_32x32x16_f16 v[80:95], v[28:31], v[132:135], v[80:95]
	v_fma_f32 v28, v6, s4, v4
	v_fma_f32 v29, v7, s4, v5
	v_cvt_f32_f16_sdwa v31, v149 dst_sel:DWORD dst_unused:UNUSED_PAD src0_sel:WORD_1
	v_cvt_f32_f16_e32 v30, v149
	ds_read_b128 v[4:7], v16
	ds_read_b128 v[16:19], v17
	ds_read_b128 v[20:23], v166 offset:43712
	ds_read_b128 v[24:27], v166 offset:35040
	s_waitcnt lgkmcnt(3)
	v_pk_add_f32 v[10:11], v[10:11], v[6:7]
	v_mfma_f32_32x32x16_f16 v[64:79], v[36:39], v[132:135], v[64:79]
	v_mfma_f32_32x32x16_f16 v[48:63], v[40:43], v[132:135], v[48:63]
	v_mfma_f32_32x32x16_f16 v[96:111], v[0:3], v[136:139], v[96:111]
	v_add_f32_e64 v0, v8, v4
	v_add_f32_e64 v1, v9, v5
	v_fma_f32 v8, v32, s4, v30
	v_fma_f32 v9, v33, s4, v31
	v_add_f32_e64 v0, v28, v0
	v_add_f32_e64 v1, v29, v1
	v_pk_add_f32 v[28:29], v[8:9], v[10:11]
	v_cvt_pk_f16_f32 v140, v0, v1
	ds_read_b128 v[0:3], v166 offset:52416
	ds_read_b128 v[4:7], v166 offset:43744
	s_waitcnt vmcnt(0)
	v_cvt_f32_f16_sdwa v31, v146 dst_sel:DWORD dst_unused:UNUSED_PAD src0_sel:WORD_1
	s_waitcnt lgkmcnt(3)
	v_mfma_f32_32x32x16_f16 v[80:95], v[20:23], v[136:139], v[80:95]
	ds_read_b128 v[8:11], v166 offset:61120
	ds_read_b128 v[20:23], v166 offset:52448
	v_cvt_f32_f16_e32 v30, v146
	v_cvt_f32_f16_sdwa v33, v142 dst_sel:DWORD dst_unused:UNUSED_PAD src0_sel:WORD_1
	v_cvt_f32_f16_e32 v32, v142
	v_cvt_pk_f16_f32 v141, v28, v29
	v_lshlrev_b32_e32 v146, 2, v164
	v_pk_fma_f32 v[28:29], v[32:33], s[4:5], v[30:31] op_sel_hi:[1,0,1]
	s_waitcnt lgkmcnt(3)
	v_mfma_f32_32x32x16_f16 v[64:79], v[0:3], v[136:139], v[64:79]
	ds_read_b128 v[0:3], v166 offset:61152
	v_cvt_f32_f16_sdwa v31, v147 dst_sel:DWORD dst_unused:UNUSED_PAD src0_sel:WORD_1
	v_cvt_f32_f16_e32 v30, v147
	v_cvt_f32_f16_sdwa v33, v143 dst_sel:DWORD dst_unused:UNUSED_PAD src0_sel:WORD_1
	v_cvt_f32_f16_e32 v32, v143
	v_lshlrev_b32_e32 v147, 2, v146
	s_waitcnt lgkmcnt(2)
	v_mfma_f32_32x32x16_f16 v[48:63], v[8:11], v[136:139], v[48:63]
	v_add_f32_e64 v8, v12, v16
	v_add_f32_e64 v9, v13, v17
	v_add_f32_e64 v10, v14, v18
	v_add_f32_e64 v11, v15, v19
	v_add_f32_e64 v8, v28, v8
	v_add_f32_e64 v9, v29, v9
	v_cvt_pk_f16_f32 v142, v8, v9
	v_pk_fma_f32 v[8:9], v[32:33], s[4:5], v[30:31] op_sel_hi:[1,0,1]
	s_load_dwordx4 s[4:7], s[0:1], 0x1f0
	v_pk_add_f32 v[8:9], v[8:9], v[10:11]
	s_nop 0
	v_cvt_pk_f16_f32 v143, v8, v9
	s_nop 1
	v_mfma_f32_32x32x16_f16 v[96:111], v[24:27], v[140:143], v[96:111]
	v_mfma_f32_32x32x16_f16 v[80:95], v[4:7], v[140:143], v[80:95]
	v_mul_u32_u24_e32 v4, 0x110, v145
	v_ashrrev_i32_e32 v145, 31, v144
	s_waitcnt lgkmcnt(0)
	v_mfma_f32_32x32x16_f16 v[64:79], v[20:23], v[140:143], v[64:79]
	v_mfma_f32_32x32x16_f16 v[48:63], v[0:3], v[140:143], v[48:63]
	s_and_saveexec_b64 s[0:1], s[8:9]
	s_cbranch_execz .LBB11_14
	v_or_b32_e32 v0, 0x21200, v147
	ds_read_b128 v[6:9], v0
	v_or_b32_e32 v2, 0x21220, v147
	ds_read_b128 v[10:13], v2
	v_lshlrev_b64 v[0:1], 5, v[144:145]
	v_lshl_add_u64 v[0:1], s[4:5], 0, v[0:1]
	s_waitcnt lgkmcnt(1)
	v_pk_add_f32 v[2:3], v[96:97], v[6:7]
	s_lshl_b64 s[4:5], s[36:37], 20
	v_cvt_pk_f16_f32 v6, v2, v3
	v_pk_add_f32 v[2:3], v[98:99], v[8:9]
	v_lshl_add_u64 v[8:9], v[0:1], 0, s[4:5]
	v_cvt_pk_f16_f32 v7, v2, v3
	v_lshlrev_b32_e32 v2, 1, v146
	v_mov_b32_e32 v3, 0
	v_lshl_add_u64 v[14:15], v[8:9], 0, v[2:3]
	global_store_dwordx2 v[14:15], v[6:7], off
	s_waitcnt lgkmcnt(0)
	v_pk_add_f32 v[6:7], v[100:101], v[10:11]
	v_or_b32_e32 v5, 0x21240, v147
	v_cvt_pk_f16_f32 v10, v6, v7
	ds_read_b128 v[6:9], v5
	v_pk_add_f32 v[12:13], v[102:103], v[12:13]
	v_or_b32_e32 v5, 0x21260, v147
	v_cvt_pk_f16_f32 v11, v12, v13
	global_store_dwordx2 v[14:15], v[10:11], off offset:16
	ds_read_b128 v[10:13], v5
	s_waitcnt lgkmcnt(1)
	v_pk_add_f32 v[6:7], v[104:105], v[6:7]
	v_pk_add_f32 v[8:9], v[106:107], v[8:9]
	s_lshl_b64 s[4:5], s[34:35], 20
	v_cvt_pk_f16_f32 v6, v6, v7
	v_cvt_pk_f16_f32 v7, v8, v9
	v_lshl_add_u64 v[8:9], v[0:1], 0, s[4:5]
	v_lshl_add_u64 v[14:15], v[8:9], 0, v[2:3]
	global_store_dwordx2 v[14:15], v[6:7], off
	s_waitcnt lgkmcnt(0)
	v_pk_add_f32 v[6:7], v[108:109], v[10:11]
	v_or_b32_e32 v5, 0x21280, v147
	v_cvt_pk_f16_f32 v10, v6, v7
	ds_read_b128 v[6:9], v5
	v_pk_add_f32 v[12:13], v[110:111], v[12:13]
	v_or_b32_e32 v5, 0x212a0, v147
	v_cvt_pk_f16_f32 v11, v12, v13
	global_store_dwordx2 v[14:15], v[10:11], off offset:16
	ds_read_b128 v[10:13], v5
	s_waitcnt lgkmcnt(1)
	v_pk_add_f32 v[6:7], v[80:81], v[6:7]
	v_pk_add_f32 v[8:9], v[82:83], v[8:9]
	s_lshl_b64 s[4:5], s[30:31], 20
	v_cvt_pk_f16_f32 v6, v6, v7
	v_cvt_pk_f16_f32 v7, v8, v9
	v_lshl_add_u64 v[8:9], v[0:1], 0, s[4:5]
	v_lshl_add_u64 v[14:15], v[8:9], 0, v[2:3]
	global_store_dwordx2 v[14:15], v[6:7], off
	s_waitcnt lgkmcnt(0)
	v_pk_add_f32 v[6:7], v[84:85], v[10:11]
	v_or_b32_e32 v5, 0x212c0, v147
	v_cvt_pk_f16_f32 v10, v6, v7
	ds_read_b128 v[6:9], v5
	v_pk_add_f32 v[12:13], v[86:87], v[12:13]
	v_or_b32_e32 v5, 0x212e0, v147
	v_cvt_pk_f16_f32 v11, v12, v13
	global_store_dwordx2 v[14:15], v[10:11], off offset:16
	ds_read_b128 v[10:13], v5
	s_waitcnt lgkmcnt(1)
	v_pk_add_f32 v[6:7], v[88:89], v[6:7]
	v_pk_add_f32 v[8:9], v[90:91], v[8:9]
	s_lshl_b64 s[4:5], s[28:29], 20
	v_cvt_pk_f16_f32 v6, v6, v7
	v_cvt_pk_f16_f32 v7, v8, v9
	v_lshl_add_u64 v[8:9], v[0:1], 0, s[4:5]
	v_lshl_add_u64 v[14:15], v[8:9], 0, v[2:3]
	global_store_dwordx2 v[14:15], v[6:7], off
	s_waitcnt lgkmcnt(0)
	v_pk_add_f32 v[6:7], v[92:93], v[10:11]
	v_or_b32_e32 v5, 0x21300, v147
	v_cvt_pk_f16_f32 v10, v6, v7
	ds_read_b128 v[6:9], v5
	v_pk_add_f32 v[12:13], v[94:95], v[12:13]
	v_or_b32_e32 v5, 0x21320, v147
	v_cvt_pk_f16_f32 v11, v12, v13
	global_store_dwordx2 v[14:15], v[10:11], off offset:16
	ds_read_b128 v[10:13], v5
	s_waitcnt lgkmcnt(1)
	v_pk_add_f32 v[6:7], v[64:65], v[6:7]
	v_pk_add_f32 v[8:9], v[66:67], v[8:9]
	s_lshl_b64 s[4:5], s[26:27], 20
	v_cvt_pk_f16_f32 v6, v6, v7
	v_cvt_pk_f16_f32 v7, v8, v9
	v_lshl_add_u64 v[8:9], v[0:1], 0, s[4:5]
	v_lshl_add_u64 v[14:15], v[8:9], 0, v[2:3]
	global_store_dwordx2 v[14:15], v[6:7], off
	s_waitcnt lgkmcnt(0)
	v_pk_add_f32 v[6:7], v[68:69], v[10:11]
	v_or_b32_e32 v5, 0x21340, v147
	v_cvt_pk_f16_f32 v10, v6, v7
	ds_read_b128 v[6:9], v5
	v_pk_add_f32 v[12:13], v[70:71], v[12:13]
	v_or_b32_e32 v5, 0x21360, v147
	v_cvt_pk_f16_f32 v11, v12, v13
	global_store_dwordx2 v[14:15], v[10:11], off offset:16
	ds_read_b128 v[10:13], v5
	s_waitcnt lgkmcnt(1)
	v_pk_add_f32 v[6:7], v[72:73], v[6:7]
	v_pk_add_f32 v[8:9], v[74:75], v[8:9]
	s_lshl_b64 s[4:5], s[24:25], 20
	v_cvt_pk_f16_f32 v6, v6, v7
	v_cvt_pk_f16_f32 v7, v8, v9
	v_lshl_add_u64 v[8:9], v[0:1], 0, s[4:5]
	v_lshl_add_u64 v[14:15], v[8:9], 0, v[2:3]
	global_store_dwordx2 v[14:15], v[6:7], off
	s_waitcnt lgkmcnt(0)
	v_pk_add_f32 v[6:7], v[76:77], v[10:11]
	v_or_b32_e32 v5, 0x21380, v147
	v_cvt_pk_f16_f32 v10, v6, v7
	ds_read_b128 v[6:9], v5
	v_pk_add_f32 v[12:13], v[78:79], v[12:13]
	v_or_b32_e32 v5, 0x213a0, v147
	v_cvt_pk_f16_f32 v11, v12, v13
	global_store_dwordx2 v[14:15], v[10:11], off offset:16
	ds_read_b128 v[10:13], v5
	s_waitcnt lgkmcnt(1)
	v_pk_add_f32 v[6:7], v[48:49], v[6:7]
	v_pk_add_f32 v[8:9], v[50:51], v[8:9]
	s_lshl_b64 s[4:5], s[10:11], 20
	v_cvt_pk_f16_f32 v6, v6, v7
	v_cvt_pk_f16_f32 v7, v8, v9
	v_lshl_add_u64 v[8:9], v[0:1], 0, s[4:5]
	v_lshl_add_u64 v[14:15], v[8:9], 0, v[2:3]
	global_store_dwordx2 v[14:15], v[6:7], off
	s_waitcnt lgkmcnt(0)
	v_pk_add_f32 v[6:7], v[52:53], v[10:11]
	v_or_b32_e32 v5, 0x213c0, v147
	v_cvt_pk_f16_f32 v10, v6, v7
	v_pk_add_f32 v[12:13], v[54:55], v[12:13]
	ds_read_b128 v[6:9], v5
	v_cvt_pk_f16_f32 v11, v12, v13
	v_or_b32_e32 v5, 0x213e0, v147
	global_store_dwordx2 v[14:15], v[10:11], off offset:16
	ds_read_b128 v[10:13], v5
	s_lshl_b64 s[4:5], s[2:3], 20
	s_waitcnt lgkmcnt(1)
	v_pk_add_f32 v[6:7], v[56:57], v[6:7]
	v_pk_add_f32 v[8:9], v[58:59], v[8:9]
	v_lshl_add_u64 v[0:1], v[0:1], 0, s[4:5]
	v_cvt_pk_f16_f32 v6, v6, v7
	v_cvt_pk_f16_f32 v7, v8, v9
	v_lshl_add_u64 v[0:1], v[0:1], 0, v[2:3]
	global_store_dwordx2 v[0:1], v[6:7], off
	s_waitcnt lgkmcnt(0)
	v_pk_add_f32 v[2:3], v[60:61], v[10:11]
	v_pk_add_f32 v[6:7], v[62:63], v[12:13]
	v_cvt_pk_f16_f32 v2, v2, v3
	v_cvt_pk_f16_f32 v3, v6, v7
	global_store_dwordx2 v[0:1], v[2:3], off offset:16

.LBB12_23:
	s_or_b64 exec, exec, s[12:13]
	s_and_saveexec_b64 s[4:5], s[6:7]
	v_mov_b32_e32 v3, 0x23600
	v_lshl_add_u32 v0, v0, 2, v3
	ds_write_b32 v0, v5
	s_or_b64 exec, exec, s[4:5]
	s_movk_i32 s3, 0x7e90
	v_cmp_gt_i32_e32 vcc, s3, v8
	s_waitcnt lgkmcnt(0)
	s_barrier
	s_and_saveexec_b64 s[4:5], vcc
	s_cbranch_execz .LBB12_30
	v_lshlrev_b32_e32 v94, 5, v164
	v_or_b32_e32 v0, 0x21c00, v94
	v_or_b32_e32 v4, 0x21e00, v94
	v_cvt_f32_i32_e32 v9, v1
	v_cvt_f32_i32_e32 v8, v2
	ds_read_b128 v[0:3], v0
	ds_read_b128 v[4:7], v4
	v_lshlrev_b32_e32 v165, 4, v164
	s_movk_i32 s3, 0x110
	v_pk_add_f32 v[92:93], v[8:9], 0.5 op_sel_hi:[1,0]
	s_waitcnt lgkmcnt(1)
	v_mov_b32_e32 v8, v0
	s_waitcnt lgkmcnt(0)
	v_mov_b32_e32 v9, v4
	v_or_b32_e32 v0, 0x22000, v94
	v_pk_mul_f32 v[20:21], v[92:93], v[8:9]
	v_or_b32_e32 v4, 0x22200, v94
	ds_read_b128 v[8:11], v0
	ds_read_b128 v[12:15], v4
	v_or_b32_e32 v0, 0x22400, v94
	ds_read_b128 v[16:19], v0
	v_add_f32_e32 v0, v20, v21
	s_waitcnt lgkmcnt(2)
	v_add_f32_e32 v0, v8, v0
	v_or_b32_e32 v4, 0x21c10, v94
	ds_read_b128 v[20:23], v4
	s_waitcnt lgkmcnt(1)
	v_fma_f32 v0, v12, v0, v16
	v_mov_b32_e32 v4, v1
	v_max_f32_e32 v24, 0, v0
	v_pk_mul_f32 v[0:1], v[92:93], v[4:5]
	v_or_b32_e32 v4, 0x22010, v94
	v_add_f32_e32 v0, v0, v1
	v_add_f32_e32 v0, v9, v0
	v_fma_f32 v0, v13, v0, v17
	v_max_f32_e32 v25, 0, v0
	v_mov_b32_e32 v0, v2
	v_mov_b32_e32 v1, v6
	v_pk_mul_f32 v[0:1], v[92:93], v[0:1]
	v_mov_b32_e32 v6, v3
	v_add_f32_e32 v0, v0, v1
	v_add_f32_e32 v0, v10, v0
	v_fma_f32 v0, v14, v0, v18
	v_max_f32_e32 v18, 0, v0
	v_pk_mul_f32 v[0:1], v[92:93], v[6:7]
	v_or_b32_e32 v8, 0x22210, v94
	v_add_f32_e32 v0, v0, v1
	v_add_f32_e32 v0, v11, v0
	v_fmac_f32_e32 v19, v15, v0
	v_or_b32_e32 v0, 0x21e10, v94
	ds_read_b128 v[0:3], v0
	ds_read_b128 v[4:7], v4
	v_or_b32_e32 v12, 0x22410, v94
	ds_read_b128 v[8:11], v8
	ds_read_b128 v[12:15], v12
	s_waitcnt lgkmcnt(4)
	v_mov_b32_e32 v16, v20
	s_waitcnt lgkmcnt(3)
	v_mov_b32_e32 v17, v0
	v_pk_mul_f32 v[16:17], v[92:93], v[16:17]
	v_mad_u32_u24 v166, v145, s3, v165
	v_add_f32_e32 v0, v16, v17
	s_waitcnt lgkmcnt(2)
	v_add_f32_e32 v0, v4, v0
	s_waitcnt lgkmcnt(0)
	v_fma_f32 v0, v8, v0, v12
	v_max_f32_e32 v4, 0, v0
	v_mov_b32_e32 v0, v21
	v_pk_mul_f32 v[0:1], v[92:93], v[0:1]
	v_max_f32_e32 v19, 0, v19
	v_add_f32_e32 v0, v0, v1
	v_add_f32_e32 v0, v5, v0
	v_fma_f32 v0, v9, v0, v13
	v_max_f32_e32 v5, 0, v0
	v_mov_b32_e32 v0, v22
	v_mov_b32_e32 v1, v2
	v_pk_mul_f32 v[0:1], v[92:93], v[0:1]
	v_mov_b32_e32 v2, v23
	v_add_f32_e32 v0, v0, v1
	v_add_f32_e32 v0, v6, v0
	v_fma_f32 v0, v10, v0, v14
	v_max_f32_e32 v6, 0, v0
	v_pk_mul_f32 v[0:1], v[92:93], v[2:3]
	ds_read_b128 v[96:99], v166 offset:32
	v_add_f32_e32 v8, v0, v1
	ds_read_b128 v[0:3], v166
	v_add_f32_e32 v7, v7, v8
	v_fmac_f32_e32 v15, v11, v7
	v_max_f32_e32 v7, 0, v15
	v_cvt_pk_f16_f32 v7, v6, v7
	v_cvt_pk_f16_f32 v6, v4, v5
	v_cvt_pk_f16_f32 v5, v18, v19
	v_cvt_pk_f16_f32 v4, v24, v25
	v_or_b32_e32 v8, 0x21c40, v94
	v_or_b32_e32 v9, 0x21e40, v94
	s_waitcnt lgkmcnt(0)
	v_mfma_f32_32x32x16_f16 v[48:63], v[0:3], v[4:7], 0
	v_mov_b32_e32 v190, 0x8180
	v_mad_i64_i32 v[192:193], s[40:41], s36, v190, v[198:199]
	v_lshlrev_b64 v[192:193], 6, v[192:193]
	v_lshl_add_u64 v[196:197], s[38:39], 0, v[192:193]
	v_mov_b32_e32 v193, 0
	v_lshlrev_b32_e32 v192, 3, v164
	v_lshl_add_u64 v[196:197], v[196:197], 0, v[192:193]
	global_load_dwordx2 v[90:91], v[196:197], off
	global_load_dwordx2 v[88:89], v[196:197], off offset:32
	global_load_dwordx2 v[84:85], v[196:197], off offset:48
	global_load_dwordx2 v[86:87], v[196:197], off offset:16
	ds_read_b128 v[0:3], v166 offset:8704
	ds_read_b128 v[100:103], v166 offset:8736
	v_or_b32_e32 v95, 0x22040, v94
	s_mov_b32 s4, 0x3a000000
	s_ashr_i32 s37, s36, 31
	s_waitcnt lgkmcnt(1)
	v_mfma_f32_32x32x16_f16 v[32:47], v[0:3], v[4:7], 0
	v_mad_i64_i32 v[196:197], s[40:41], s34, v190, v[198:199]
	v_lshlrev_b64 v[196:197], 6, v[196:197]
	v_lshl_add_u64 v[196:197], s[38:39], 0, v[196:197]
	v_lshl_add_u64 v[196:197], v[196:197], 0, v[192:193]
	global_load_dwordx2 v[82:83], v[196:197], off
	global_load_dwordx2 v[80:81], v[196:197], off offset:32
	global_load_dwordx2 v[76:77], v[196:197], off offset:48
	global_load_dwordx2 v[78:79], v[196:197], off offset:16
	ds_read_b128 v[0:3], v166 offset:17408
	ds_read_b128 v[104:107], v166 offset:17440
	s_ashr_i32 s35, s34, 31
	s_ashr_i32 s31, s30, 31
	s_ashr_i32 s29, s28, 31
	s_ashr_i32 s27, s26, 31
	s_ashr_i32 s25, s24, 31
	s_ashr_i32 s11, s10, 31
	s_waitcnt lgkmcnt(1)
	v_mfma_f32_32x32x16_f16 v[16:31], v[0:3], v[4:7], 0
	v_mad_i64_i32 v[196:197], s[40:41], s30, v190, v[198:199]
	v_lshlrev_b64 v[196:197], 6, v[196:197]
	v_lshl_add_u64 v[196:197], s[38:39], 0, v[196:197]
	v_lshl_add_u64 v[196:197], v[196:197], 0, v[192:193]
	global_load_dwordx2 v[74:75], v[196:197], off
	global_load_dwordx2 v[72:73], v[196:197], off offset:32
	global_load_dwordx2 v[68:69], v[196:197], off offset:48
	global_load_dwordx2 v[70:71], v[196:197], off offset:16
	ds_read_b128 v[0:3], v166 offset:26112
	ds_read_b128 v[108:111], v8
	ds_read_b128 v[112:115], v9
	ds_read_b128 v[116:119], v166 offset:26144
	s_ashr_i32 s3, s2, 31
	s_waitcnt lgkmcnt(2)
	v_mov_b32_e32 v120, v108
	s_waitcnt lgkmcnt(1)
	v_mov_b32_e32 v121, v112
	v_pk_mul_f32 v[124:125], v[92:93], v[120:121]
	v_or_b32_e32 v108, 0x22240, v94
	ds_read_b128 v[120:123], v95
	ds_read_b128 v[168:171], v108
	v_or_b32_e32 v95, 0x22440, v94
	ds_read_b128 v[172:175], v95
	v_or_b32_e32 v108, 0x21c50, v94
	v_mov_b32_e32 v112, v109
	ds_read_b128 v[176:179], v108
	v_pk_mul_f32 v[108:109], v[92:93], v[112:113]
	v_add_f32_e32 v95, v124, v125
	v_add_f32_e32 v108, v108, v109
	s_waitcnt lgkmcnt(3)
	v_add_f32_e32 v108, v121, v108
	s_waitcnt lgkmcnt(1)
	v_fma_f32 v108, v169, v108, v173
	v_max_f32_e32 v167, 0, v108
	v_mov_b32_e32 v108, v110
	v_mov_b32_e32 v109, v114
	v_pk_mul_f32 v[108:109], v[92:93], v[108:109]
	v_add_f32_e32 v95, v120, v95
	v_add_f32_e32 v108, v108, v109
	v_add_f32_e32 v108, v122, v108
	v_fma_f32 v108, v170, v108, v174
	v_mov_b32_e32 v114, v111
	v_fma_f32 v95, v168, v95, v172
	v_max_f32_e32 v172, 0, v108
	v_pk_mul_f32 v[108:109], v[92:93], v[114:115]
	v_or_b32_e32 v112, 0x22050, v94
	v_add_f32_e32 v108, v108, v109
	v_add_f32_e32 v108, v123, v108
	v_fmac_f32_e32 v175, v171, v108
	v_or_b32_e32 v108, 0x21e50, v94
	ds_read_b128 v[108:111], v108
	ds_read_b128 v[112:115], v112
	v_or_b32_e32 v120, 0x22250, v94
	v_or_b32_e32 v125, 0x22450, v94
	ds_read_b128 v[120:123], v120
	ds_read_b128 v[168:171], v125
	s_waitcnt lgkmcnt(4)
	v_mov_b32_e32 v124, v176
	s_waitcnt lgkmcnt(3)
	v_mov_b32_e32 v125, v108
	v_pk_mul_f32 v[124:125], v[92:93], v[124:125]
	v_max_f32_e32 v95, 0, v95
	v_add_f32_e32 v108, v124, v125
	s_waitcnt lgkmcnt(2)
	v_add_f32_e32 v108, v112, v108
	s_waitcnt lgkmcnt(0)
	v_fma_f32 v108, v120, v108, v168
	v_max_f32_e32 v112, 0, v108
	v_mov_b32_e32 v108, v177
	v_pk_mul_f32 v[108:109], v[92:93], v[108:109]
	v_max_f32_e32 v173, 0, v175
	v_add_f32_e32 v108, v108, v109
	v_add_f32_e32 v108, v113, v108
	v_fma_f32 v108, v121, v108, v169
	v_max_f32_e32 v113, 0, v108
	v_mov_b32_e32 v108, v178
	v_mov_b32_e32 v109, v110
	v_pk_mul_f32 v[108:109], v[92:93], v[108:109]
	v_mov_b32_e32 v110, v179
	v_add_f32_e32 v108, v108, v109
	v_add_f32_e32 v108, v114, v108
	v_fma_f32 v108, v122, v108, v170
	v_max_f32_e32 v114, 0, v108
	v_pk_mul_f32 v[108:109], v[92:93], v[110:111]
	v_mfma_f32_32x32x16_f16 v[0:15], v[0:3], v[4:7], 0
	v_mad_i64_i32 v[196:197], s[40:41], s28, v190, v[198:199]
	v_lshlrev_b64 v[196:197], 6, v[196:197]
	v_lshl_add_u64 v[196:197], s[38:39], 0, v[196:197]
	v_lshl_add_u64 v[196:197], v[196:197], 0, v[192:193]
	global_load_dwordx2 v[66:67], v[196:197], off
	global_load_dwordx2 v[64:65], v[196:197], off offset:32
	global_load_dwordx2 v[126:127], v[196:197], off offset:48
	global_load_dwordx2 v[162:163], v[196:197], off offset:16
	v_add_f32_e32 v108, v108, v109
	v_add_f32_e32 v108, v115, v108
	v_fmac_f32_e32 v171, v123, v108
	v_max_f32_e32 v108, 0, v171
	v_cvt_pk_f16_f32 v111, v114, v108
	v_cvt_pk_f16_f32 v110, v112, v113
	v_cvt_pk_f16_f32 v109, v172, v173
	v_cvt_pk_f16_f32 v108, v95, v167
	v_or_b32_e32 v95, 0x21c80, v94
	s_nop 0
	v_mfma_f32_32x32x16_f16 v[32:47], v[100:103], v[108:111], v[32:47]
	v_mad_i64_i32 v[196:197], s[40:41], s26, v190, v[198:199]
	v_lshlrev_b64 v[196:197], 6, v[196:197]
	v_lshl_add_u64 v[196:197], s[38:39], 0, v[196:197]
	v_lshl_add_u64 v[196:197], v[196:197], 0, v[192:193]
	global_load_dwordx2 v[160:161], v[196:197], off
	global_load_dwordx2 v[128:129], v[196:197], off offset:32
	global_load_dwordx2 v[130:131], v[196:197], off offset:48
	global_load_dwordx2 v[158:159], v[196:197], off offset:16
	v_or_b32_e32 v100, 0x21e80, v94
	v_mfma_f32_32x32x16_f16 v[48:63], v[96:99], v[108:111], v[48:63]
	v_mad_i64_i32 v[196:197], s[40:41], s24, v190, v[198:199]
	v_lshlrev_b64 v[196:197], 6, v[196:197]
	v_lshl_add_u64 v[196:197], s[38:39], 0, v[196:197]
	v_lshl_add_u64 v[196:197], v[196:197], 0, v[192:193]
	global_load_dwordx2 v[156:157], v[196:197], off
	global_load_dwordx2 v[132:133], v[196:197], off offset:32
	global_load_dwordx2 v[134:135], v[196:197], off offset:48
	global_load_dwordx2 v[154:155], v[196:197], off offset:16
	ds_read_b128 v[96:99], v95
	ds_read_b128 v[100:103], v100
	v_or_b32_e32 v95, 0x22080, v94
	v_mfma_f32_32x32x16_f16 v[16:31], v[104:107], v[108:111], v[16:31]
	v_mad_i64_i32 v[196:197], s[40:41], s10, v190, v[198:199]
	v_mad_i64_i32 v[198:199], s[40:41], s2, v190, v[198:199]
	v_lshlrev_b64 v[196:197], 6, v[196:197]
	v_lshlrev_b64 v[198:199], 6, v[198:199]
	v_lshl_add_u64 v[196:197], s[38:39], 0, v[196:197]
	v_lshl_add_u64 v[198:199], s[38:39], 0, v[198:199]
	v_lshl_add_u64 v[196:197], v[196:197], 0, v[192:193]
	v_lshl_add_u64 v[198:199], v[198:199], 0, v[192:193]
	global_load_dwordx2 v[152:153], v[196:197], off
	global_load_dwordx2 v[136:137], v[196:197], off offset:32
	global_load_dwordx2 v[138:139], v[196:197], off offset:48
	global_load_dwordx2 v[150:151], v[196:197], off offset:16
	global_load_dwordx2 v[148:149], v[198:199], off
	global_load_dwordx2 v[140:141], v[198:199], off offset:32
	global_load_dwordx2 v[142:143], v[198:199], off offset:48
	global_load_dwordx2 v[146:147], v[198:199], off offset:16
	s_waitcnt lgkmcnt(1)
	v_mov_b32_e32 v104, v96
	s_waitcnt lgkmcnt(0)
	v_mov_b32_e32 v105, v100
	v_or_b32_e32 v96, 0x22280, v94
	v_mov_b32_e32 v100, v97
	v_mfma_f32_32x32x16_f16 v[0:15], v[116:119], v[108:111], v[0:15]
	v_mul_f32_e64 v116, v92, v104
	v_mul_f32_e64 v117, v93, v105
	ds_read_b128 v[104:107], v95
	ds_read_b128 v[108:111], v96
	v_or_b32_e32 v95, 0x22480, v94
	ds_read_b128 v[112:115], v95
	v_or_b32_e32 v96, 0x21c90, v94
	v_add_f32_e32 v95, v116, v117
	ds_read_b128 v[116:119], v96
	v_pk_mul_f32 v[96:97], v[92:93], v[100:101]
	v_or_b32_e32 v100, 0x22090, v94
	v_add_f32_e32 v96, v96, v97
	s_waitcnt lgkmcnt(3)
	v_add_f32_e32 v96, v105, v96
	s_waitcnt lgkmcnt(1)
	v_fma_f32 v96, v109, v96, v113
	v_max_f32_e32 v120, 0, v96
	v_mov_b32_e32 v96, v98
	v_mov_b32_e32 v97, v102
	v_pk_mul_f32 v[96:97], v[92:93], v[96:97]
	v_mov_b32_e32 v102, v99
	v_add_f32_e32 v96, v96, v97
	v_add_f32_e32 v96, v106, v96
	v_fma_f32 v96, v110, v96, v114
	v_max_f32_e32 v114, 0, v96
	v_pk_mul_f32 v[96:97], v[92:93], v[102:103]
	v_add_f32_e32 v95, v104, v95
	v_add_f32_e32 v96, v96, v97
	v_add_f32_e32 v96, v107, v96
	v_fmac_f32_e32 v115, v111, v96
	v_or_b32_e32 v96, 0x21e90, v94
	ds_read_b128 v[96:99], v96
	ds_read_b128 v[100:103], v100
	v_fma_f32 v95, v108, v95, v112
	v_or_b32_e32 v104, 0x22290, v94
	v_or_b32_e32 v108, 0x22490, v94
	ds_read_b128 v[104:107], v104
	ds_read_b128 v[108:111], v108
	s_waitcnt lgkmcnt(4)
	v_mov_b32_e32 v112, v116
	s_waitcnt lgkmcnt(3)
	v_mov_b32_e32 v113, v96
	v_pk_mul_f32 v[112:113], v[92:93], v[112:113]
	v_max_f32_e32 v95, 0, v95
	v_add_f32_e32 v96, v112, v113
	s_waitcnt lgkmcnt(2)
	v_add_f32_e32 v96, v100, v96
	s_waitcnt lgkmcnt(0)
	v_fma_f32 v96, v104, v96, v108
	v_max_f32_e32 v100, 0, v96
	v_mov_b32_e32 v96, v117
	v_pk_mul_f32 v[96:97], v[92:93], v[96:97]
	v_max_f32_e32 v115, 0, v115
	v_add_f32_e32 v96, v96, v97
	v_add_f32_e32 v96, v101, v96
	v_fma_f32 v96, v105, v96, v109
	v_max_f32_e32 v101, 0, v96
	v_mov_b32_e32 v96, v118
	v_mov_b32_e32 v97, v98
	v_pk_mul_f32 v[96:97], v[92:93], v[96:97]
	v_mov_b32_e32 v98, v119
	v_add_f32_e32 v96, v96, v97
	v_add_f32_e32 v96, v102, v96
	v_fma_f32 v96, v106, v96, v110
	v_max_f32_e32 v102, 0, v96
	v_pk_mul_f32 v[96:97], v[92:93], v[98:99]
	s_nop 0
	v_add_f32_e32 v104, v96, v97
	ds_read_b128 v[96:99], v166 offset:64
	v_add_f32_e32 v103, v103, v104
	v_fmac_f32_e32 v111, v107, v103
	v_max_f32_e32 v103, 0, v111
	v_cvt_pk_f16_f32 v103, v102, v103
	v_cvt_pk_f16_f32 v102, v100, v101
	v_cvt_pk_f16_f32 v101, v114, v115
	v_cvt_pk_f16_f32 v100, v95, v120
	ds_read_b128 v[104:107], v166 offset:96
	v_or_b32_e32 v95, 0x21cc0, v94
	s_waitcnt lgkmcnt(1)
	v_mfma_f32_32x32x16_f16 v[48:63], v[96:99], v[100:103], v[48:63]
	ds_read_b128 v[96:99], v166 offset:8768
	ds_read_b128 v[108:111], v166 offset:8800
	v_or_b32_e32 v120, 0x21ec0, v94
	s_waitcnt lgkmcnt(1)
	v_mfma_f32_32x32x16_f16 v[32:47], v[96:99], v[100:103], v[32:47]
	ds_read_b128 v[96:99], v166 offset:17472
	ds_read_b128 v[112:115], v166 offset:17504
	s_waitcnt lgkmcnt(1)
	v_mfma_f32_32x32x16_f16 v[16:31], v[96:99], v[100:103], v[16:31]
	ds_read_b128 v[96:99], v166 offset:26176
	ds_read_b128 v[116:119], v95
	ds_read_b128 v[120:123], v120
	ds_read_b128 v[168:171], v166 offset:26208
	v_or_b32_e32 v95, 0x220c0, v94
	s_waitcnt lgkmcnt(3)
	v_mfma_f32_32x32x16_f16 v[0:15], v[96:99], v[100:103], v[0:15]
	s_waitcnt lgkmcnt(2)
	v_mov_b32_e32 v96, v116
	s_waitcnt lgkmcnt(1)
	v_mov_b32_e32 v97, v120
	v_or_b32_e32 v100, 0x222c0, v94
	v_pk_mul_f32 v[124:125], v[92:93], v[96:97]
	ds_read_b128 v[96:99], v95
	ds_read_b128 v[100:103], v100
	v_or_b32_e32 v95, 0x224c0, v94
	ds_read_b128 v[172:175], v95
	v_add_f32_e32 v95, v124, v125
	v_mov_b32_e32 v120, v117
	s_waitcnt lgkmcnt(2)
	v_add_f32_e32 v95, v96, v95
	v_or_b32_e32 v96, 0x21cd0, v94
	v_pk_mul_f32 v[116:117], v[92:93], v[120:121]
	ds_read_b128 v[176:179], v96
	v_add_f32_e32 v96, v116, v117
	v_add_f32_e32 v96, v97, v96
	s_waitcnt lgkmcnt(1)
	v_fma_f32 v96, v101, v96, v173
	v_max_f32_e32 v167, 0, v96
	v_mov_b32_e32 v96, v118
	v_mov_b32_e32 v97, v122
	v_pk_mul_f32 v[96:97], v[92:93], v[96:97]
	v_mov_b32_e32 v122, v119
	v_add_f32_e32 v96, v96, v97
	v_add_f32_e32 v96, v98, v96
	v_fma_f32 v96, v102, v96, v174
	v_fma_f32 v95, v100, v95, v172
	v_max_f32_e32 v172, 0, v96
	v_pk_mul_f32 v[96:97], v[92:93], v[122:123]
	v_or_b32_e32 v100, 0x220d0, v94
	v_add_f32_e32 v96, v96, v97
	v_add_f32_e32 v96, v99, v96
	v_fmac_f32_e32 v175, v103, v96
	v_or_b32_e32 v96, 0x21ed0, v94
	ds_read_b128 v[96:99], v96
	ds_read_b128 v[100:103], v100
	v_or_b32_e32 v116, 0x222d0, v94
	v_or_b32_e32 v120, 0x224d0, v94
	ds_read_b128 v[116:119], v116
	ds_read_b128 v[120:123], v120
	s_waitcnt lgkmcnt(4)
	v_mov_b32_e32 v124, v176
	s_waitcnt lgkmcnt(3)
	v_mov_b32_e32 v125, v96
	v_pk_mul_f32 v[124:125], v[92:93], v[124:125]
	v_max_f32_e32 v95, 0, v95
	v_add_f32_e32 v96, v124, v125
	s_waitcnt lgkmcnt(2)
	v_add_f32_e32 v96, v100, v96
	s_waitcnt lgkmcnt(0)
	v_fma_f32 v96, v116, v96, v120
	v_max_f32_e32 v100, 0, v96
	v_mov_b32_e32 v96, v177
	v_pk_mul_f32 v[96:97], v[92:93], v[96:97]
	v_max_f32_e32 v173, 0, v175
	v_add_f32_e32 v96, v96, v97
	v_add_f32_e32 v96, v101, v96
	v_fma_f32 v96, v117, v96, v121
	v_max_f32_e32 v101, 0, v96
	v_mov_b32_e32 v96, v178
	v_mov_b32_e32 v97, v98
	v_pk_mul_f32 v[96:97], v[92:93], v[96:97]
	v_mov_b32_e32 v98, v179
	v_add_f32_e32 v96, v96, v97
	v_add_f32_e32 v96, v102, v96
	v_fma_f32 v96, v118, v96, v122
	v_max_f32_e32 v102, 0, v96
	v_pk_mul_f32 v[96:97], v[92:93], v[98:99]
	v_cvt_pk_f16_f32 v98, v100, v101
	v_add_f32_e32 v96, v96, v97
	v_add_f32_e32 v96, v103, v96
	v_fmac_f32_e32 v123, v119, v96
	v_max_f32_e32 v96, 0, v123
	v_cvt_pk_f16_f32 v99, v102, v96
	v_cvt_pk_f16_f32 v97, v172, v173
	v_cvt_pk_f16_f32 v96, v95, v167
	v_or_b32_e32 v95, 0x21d00, v94
	s_nop 0
	v_mfma_f32_32x32x16_f16 v[48:63], v[104:107], v[96:99], v[48:63]
	v_or_b32_e32 v104, 0x21f00, v94
	ds_read_b128 v[100:103], v95
	ds_read_b128 v[104:107], v104
	v_or_b32_e32 v95, 0x22100, v94
	v_mfma_f32_32x32x16_f16 v[32:47], v[108:111], v[96:99], v[32:47]
	v_mfma_f32_32x32x16_f16 v[16:31], v[112:115], v[96:99], v[16:31]
	v_mfma_f32_32x32x16_f16 v[0:15], v[168:171], v[96:99], v[0:15]
	s_waitcnt lgkmcnt(1)
	v_mov_b32_e32 v96, v100
	s_waitcnt lgkmcnt(0)
	v_mov_b32_e32 v97, v104
	v_mul_f32_e64 v116, v92, v96
	v_mul_f32_e64 v117, v93, v97
	v_or_b32_e32 v100, 0x22300, v94
	ds_read_b128 v[96:99], v95
	ds_read_b128 v[108:111], v100
	v_or_b32_e32 v95, 0x22500, v94
	ds_read_b128 v[112:115], v95
	v_add_f32_e32 v95, v116, v117
	v_mov_b32_e32 v104, v101
	s_waitcnt lgkmcnt(2)
	v_add_f32_e32 v95, v96, v95
	v_or_b32_e32 v96, 0x21d10, v94
	v_pk_mul_f32 v[100:101], v[92:93], v[104:105]
	ds_read_b128 v[116:119], v96
	v_add_f32_e32 v96, v100, v101
	v_add_f32_e32 v96, v97, v96
	s_waitcnt lgkmcnt(1)
	v_fma_f32 v96, v109, v96, v113
	v_max_f32_e32 v120, 0, v96
	v_mov_b32_e32 v96, v102
	v_mov_b32_e32 v97, v106
	v_pk_mul_f32 v[96:97], v[92:93], v[96:97]
	v_mov_b32_e32 v106, v103
	v_add_f32_e32 v96, v96, v97
	v_add_f32_e32 v96, v98, v96
	v_fma_f32 v96, v110, v96, v114
	v_max_f32_e32 v114, 0, v96
	v_pk_mul_f32 v[96:97], v[92:93], v[106:107]
	v_or_b32_e32 v100, 0x22110, v94
	v_add_f32_e32 v96, v96, v97
	v_add_f32_e32 v96, v99, v96
	v_fmac_f32_e32 v115, v111, v96
	v_or_b32_e32 v96, 0x21f10, v94
	ds_read_b128 v[96:99], v96
	ds_read_b128 v[100:103], v100
	v_fma_f32 v95, v108, v95, v112
	v_or_b32_e32 v104, 0x22310, v94
	v_or_b32_e32 v108, 0x22510, v94
	ds_read_b128 v[104:107], v104
	ds_read_b128 v[108:111], v108
	s_waitcnt lgkmcnt(4)
	v_mov_b32_e32 v112, v116
	s_waitcnt lgkmcnt(3)
	v_mov_b32_e32 v113, v96
	v_pk_mul_f32 v[112:113], v[92:93], v[112:113]
	v_max_f32_e32 v95, 0, v95
	v_add_f32_e32 v96, v112, v113
	s_waitcnt lgkmcnt(2)
	v_add_f32_e32 v96, v100, v96
	s_waitcnt lgkmcnt(0)
	v_fma_f32 v96, v104, v96, v108
	v_max_f32_e32 v100, 0, v96
	v_mov_b32_e32 v96, v117
	v_pk_mul_f32 v[96:97], v[92:93], v[96:97]
	v_max_f32_e32 v115, 0, v115
	v_add_f32_e32 v96, v96, v97
	v_add_f32_e32 v96, v101, v96
	v_fma_f32 v96, v105, v96, v109
	v_max_f32_e32 v101, 0, v96
	v_mov_b32_e32 v96, v118
	v_mov_b32_e32 v97, v98
	v_pk_mul_f32 v[96:97], v[92:93], v[96:97]
	v_mov_b32_e32 v98, v119
	v_add_f32_e32 v96, v96, v97
	v_add_f32_e32 v96, v102, v96
	v_fma_f32 v96, v106, v96, v110
	v_max_f32_e32 v102, 0, v96
	v_pk_mul_f32 v[96:97], v[92:93], v[98:99]
	s_nop 0
	v_add_f32_e32 v104, v96, v97
	ds_read_b128 v[96:99], v166 offset:128
	v_add_f32_e32 v103, v103, v104
	v_fmac_f32_e32 v111, v107, v103
	v_max_f32_e32 v103, 0, v111
	v_cvt_pk_f16_f32 v103, v102, v103
	v_cvt_pk_f16_f32 v102, v100, v101
	v_cvt_pk_f16_f32 v101, v114, v115
	v_cvt_pk_f16_f32 v100, v95, v120
	ds_read_b128 v[104:107], v166 offset:160
	v_or_b32_e32 v95, 0x21d40, v94
	s_waitcnt lgkmcnt(1)
	v_mfma_f32_32x32x16_f16 v[48:63], v[96:99], v[100:103], v[48:63]
	ds_read_b128 v[96:99], v166 offset:8832
	ds_read_b128 v[108:111], v166 offset:8864
	v_or_b32_e32 v120, 0x21f40, v94
	s_waitcnt lgkmcnt(1)
	v_mfma_f32_32x32x16_f16 v[32:47], v[96:99], v[100:103], v[32:47]
	ds_read_b128 v[96:99], v166 offset:17536
	ds_read_b128 v[112:115], v166 offset:17568
	s_waitcnt lgkmcnt(1)
	v_mfma_f32_32x32x16_f16 v[16:31], v[96:99], v[100:103], v[16:31]
	ds_read_b128 v[96:99], v166 offset:26240
	ds_read_b128 v[116:119], v95
	ds_read_b128 v[120:123], v120
	ds_read_b128 v[168:171], v166 offset:26272
	v_or_b32_e32 v95, 0x22140, v94
	s_waitcnt lgkmcnt(3)
	v_mfma_f32_32x32x16_f16 v[0:15], v[96:99], v[100:103], v[0:15]
	s_waitcnt lgkmcnt(2)
	v_mov_b32_e32 v96, v116
	s_waitcnt lgkmcnt(1)
	v_mov_b32_e32 v97, v120
	v_or_b32_e32 v100, 0x22340, v94
	v_pk_mul_f32 v[124:125], v[92:93], v[96:97]
	ds_read_b128 v[96:99], v95
	ds_read_b128 v[100:103], v100
	v_or_b32_e32 v95, 0x22540, v94
	ds_read_b128 v[172:175], v95
	v_add_f32_e32 v95, v124, v125
	v_mov_b32_e32 v120, v117
	s_waitcnt lgkmcnt(2)
	v_add_f32_e32 v95, v96, v95
	v_or_b32_e32 v96, 0x21d50, v94
	v_pk_mul_f32 v[116:117], v[92:93], v[120:121]
	ds_read_b128 v[176:179], v96
	v_add_f32_e32 v96, v116, v117
	v_add_f32_e32 v96, v97, v96
	s_waitcnt lgkmcnt(1)
	v_fma_f32 v96, v101, v96, v173
	v_max_f32_e32 v167, 0, v96
	v_mov_b32_e32 v96, v118
	v_mov_b32_e32 v97, v122
	v_pk_mul_f32 v[96:97], v[92:93], v[96:97]
	v_mov_b32_e32 v122, v119
	v_add_f32_e32 v96, v96, v97
	v_add_f32_e32 v96, v98, v96
	v_fma_f32 v96, v102, v96, v174
	v_fma_f32 v95, v100, v95, v172
	v_max_f32_e32 v172, 0, v96
	v_pk_mul_f32 v[96:97], v[92:93], v[122:123]
	v_or_b32_e32 v100, 0x22150, v94
	v_add_f32_e32 v96, v96, v97
	v_add_f32_e32 v96, v99, v96
	v_fmac_f32_e32 v175, v103, v96
	v_or_b32_e32 v96, 0x21f50, v94
	ds_read_b128 v[96:99], v96
	ds_read_b128 v[100:103], v100
	v_or_b32_e32 v116, 0x22350, v94
	v_or_b32_e32 v120, 0x22550, v94
	ds_read_b128 v[116:119], v116
	ds_read_b128 v[120:123], v120
	s_waitcnt lgkmcnt(4)
	v_mov_b32_e32 v124, v176
	s_waitcnt lgkmcnt(3)
	v_mov_b32_e32 v125, v96
	v_pk_mul_f32 v[124:125], v[92:93], v[124:125]
	v_max_f32_e32 v95, 0, v95
	v_add_f32_e32 v96, v124, v125
	s_waitcnt lgkmcnt(2)
	v_add_f32_e32 v96, v100, v96
	s_waitcnt lgkmcnt(0)
	v_fma_f32 v96, v116, v96, v120
	v_max_f32_e32 v100, 0, v96
	v_mov_b32_e32 v96, v177
	v_pk_mul_f32 v[96:97], v[92:93], v[96:97]
	v_max_f32_e32 v173, 0, v175
	v_add_f32_e32 v96, v96, v97
	v_add_f32_e32 v96, v101, v96
	v_fma_f32 v96, v117, v96, v121
	v_max_f32_e32 v101, 0, v96
	v_mov_b32_e32 v96, v178
	v_mov_b32_e32 v97, v98
	v_pk_mul_f32 v[96:97], v[92:93], v[96:97]
	v_mov_b32_e32 v98, v179
	v_add_f32_e32 v96, v96, v97
	v_add_f32_e32 v96, v102, v96
	v_fma_f32 v96, v118, v96, v122
	v_max_f32_e32 v102, 0, v96
	v_pk_mul_f32 v[96:97], v[92:93], v[98:99]
	v_cvt_pk_f16_f32 v98, v100, v101
	v_add_f32_e32 v96, v96, v97
	v_add_f32_e32 v96, v103, v96
	v_fmac_f32_e32 v123, v119, v96
	v_max_f32_e32 v96, 0, v123
	v_cvt_pk_f16_f32 v99, v102, v96
	v_cvt_pk_f16_f32 v97, v172, v173
	v_cvt_pk_f16_f32 v96, v95, v167
	v_or_b32_e32 v95, 0x21d80, v94
	s_nop 0
	v_mfma_f32_32x32x16_f16 v[48:63], v[104:107], v[96:99], v[48:63]
	v_or_b32_e32 v104, 0x21f80, v94
	ds_read_b128 v[100:103], v95
	ds_read_b128 v[104:107], v104
	v_or_b32_e32 v95, 0x22180, v94
	v_mfma_f32_32x32x16_f16 v[32:47], v[108:111], v[96:99], v[32:47]
	v_mfma_f32_32x32x16_f16 v[16:31], v[112:115], v[96:99], v[16:31]
	v_mfma_f32_32x32x16_f16 v[0:15], v[168:171], v[96:99], v[0:15]
	s_waitcnt lgkmcnt(1)
	v_mov_b32_e32 v96, v100
	s_waitcnt lgkmcnt(0)
	v_mov_b32_e32 v97, v104
	v_mul_f32_e64 v116, v92, v96
	v_mul_f32_e64 v117, v93, v97
	v_or_b32_e32 v100, 0x22380, v94
	ds_read_b128 v[96:99], v95
	ds_read_b128 v[108:111], v100
	v_or_b32_e32 v95, 0x22580, v94
	ds_read_b128 v[112:115], v95
	v_add_f32_e32 v95, v116, v117
	v_mov_b32_e32 v104, v101
	s_waitcnt lgkmcnt(2)
	v_add_f32_e32 v95, v96, v95
	v_or_b32_e32 v96, 0x21d90, v94
	v_pk_mul_f32 v[100:101], v[92:93], v[104:105]
	ds_read_b128 v[116:119], v96
	v_add_f32_e32 v96, v100, v101
	v_add_f32_e32 v96, v97, v96
	s_waitcnt lgkmcnt(1)
	v_fma_f32 v96, v109, v96, v113
	v_max_f32_e32 v120, 0, v96
	v_mov_b32_e32 v96, v102
	v_mov_b32_e32 v97, v106
	v_pk_mul_f32 v[96:97], v[92:93], v[96:97]
	v_mov_b32_e32 v106, v103
	v_add_f32_e32 v96, v96, v97
	v_add_f32_e32 v96, v98, v96
	v_fma_f32 v96, v110, v96, v114
	v_max_f32_e32 v114, 0, v96
	v_pk_mul_f32 v[96:97], v[92:93], v[106:107]
	v_or_b32_e32 v100, 0x22190, v94
	v_add_f32_e32 v96, v96, v97
	v_add_f32_e32 v96, v99, v96
	v_fmac_f32_e32 v115, v111, v96
	v_or_b32_e32 v96, 0x21f90, v94
	ds_read_b128 v[96:99], v96
	ds_read_b128 v[100:103], v100
	v_fma_f32 v95, v108, v95, v112
	v_or_b32_e32 v104, 0x22390, v94
	v_or_b32_e32 v108, 0x22590, v94
	ds_read_b128 v[104:107], v104
	ds_read_b128 v[108:111], v108
	s_waitcnt lgkmcnt(4)
	v_mov_b32_e32 v112, v116
	s_waitcnt lgkmcnt(3)
	v_mov_b32_e32 v113, v96
	v_pk_mul_f32 v[112:113], v[92:93], v[112:113]
	v_max_f32_e32 v95, 0, v95
	v_add_f32_e32 v96, v112, v113
	s_waitcnt lgkmcnt(2)
	v_add_f32_e32 v96, v100, v96
	s_waitcnt lgkmcnt(0)
	v_fma_f32 v96, v104, v96, v108
	v_max_f32_e32 v100, 0, v96
	v_mov_b32_e32 v96, v117
	v_pk_mul_f32 v[96:97], v[92:93], v[96:97]
	v_max_f32_e32 v115, 0, v115
	v_add_f32_e32 v96, v96, v97
	v_add_f32_e32 v96, v101, v96
	v_fma_f32 v96, v105, v96, v109
	v_max_f32_e32 v101, 0, v96
	v_mov_b32_e32 v96, v118
	v_mov_b32_e32 v97, v98
	v_pk_mul_f32 v[96:97], v[92:93], v[96:97]
	v_mov_b32_e32 v98, v119
	v_add_f32_e32 v96, v96, v97
	v_add_f32_e32 v96, v102, v96
	v_fma_f32 v96, v106, v96, v110
	v_max_f32_e32 v102, 0, v96
	v_pk_mul_f32 v[96:97], v[92:93], v[98:99]
	s_nop 0
	v_add_f32_e32 v104, v96, v97
	ds_read_b128 v[96:99], v166 offset:192
	v_add_f32_e32 v103, v103, v104
	v_fmac_f32_e32 v111, v107, v103
	v_max_f32_e32 v103, 0, v111
	v_cvt_pk_f16_f32 v103, v102, v103
	v_cvt_pk_f16_f32 v102, v100, v101
	v_cvt_pk_f16_f32 v101, v114, v115
	v_cvt_pk_f16_f32 v100, v95, v120
	ds_read_b128 v[104:107], v166 offset:224
	v_or_b32_e32 v95, 0x21dc0, v94
	s_waitcnt lgkmcnt(1)
	v_mfma_f32_32x32x16_f16 v[48:63], v[96:99], v[100:103], v[48:63]
	ds_read_b128 v[96:99], v166 offset:8896
	ds_read_b128 v[108:111], v166 offset:8928
	v_or_b32_e32 v120, 0x21fc0, v94
	s_waitcnt lgkmcnt(1)
	v_mfma_f32_32x32x16_f16 v[32:47], v[96:99], v[100:103], v[32:47]
	ds_read_b128 v[96:99], v166 offset:17600
	ds_read_b128 v[112:115], v166 offset:17632
	s_waitcnt lgkmcnt(1)
	v_mfma_f32_32x32x16_f16 v[16:31], v[96:99], v[100:103], v[16:31]
	ds_read_b128 v[96:99], v166 offset:26304
	ds_read_b128 v[116:119], v95
	ds_read_b128 v[120:123], v120
	ds_read_b128 v[168:171], v166 offset:26336
	v_or_b32_e32 v95, 0x221c0, v94
	s_waitcnt lgkmcnt(3)
	v_mfma_f32_32x32x16_f16 v[0:15], v[96:99], v[100:103], v[0:15]
	s_waitcnt lgkmcnt(2)
	v_mov_b32_e32 v96, v116
	s_waitcnt lgkmcnt(1)
	v_mov_b32_e32 v97, v120
	v_or_b32_e32 v100, 0x223c0, v94
	v_pk_mul_f32 v[124:125], v[92:93], v[96:97]
	ds_read_b128 v[96:99], v95
	ds_read_b128 v[100:103], v100
	v_or_b32_e32 v95, 0x225c0, v94
	ds_read_b128 v[172:175], v95
	v_add_f32_e32 v95, v124, v125
	s_waitcnt lgkmcnt(2)
	v_add_f32_e32 v95, v96, v95
	v_mov_b32_e32 v120, v117
	v_pk_mul_f32 v[116:117], v[92:93], v[120:121]
	s_waitcnt lgkmcnt(0)
	v_fma_f32 v95, v100, v95, v172
	v_or_b32_e32 v96, 0x21dd0, v94
	v_max_f32_e32 v167, 0, v95
	v_add_f32_e32 v95, v116, v117
	ds_read_b128 v[176:179], v96
	v_add_f32_e32 v95, v97, v95
	v_mov_b32_e32 v96, v118
	v_mov_b32_e32 v97, v122
	v_fma_f32 v95, v101, v95, v173
	v_pk_mul_f32 v[96:97], v[92:93], v[96:97]
	v_max_f32_e32 v172, 0, v95
	v_add_f32_e32 v95, v96, v97
	v_add_f32_e32 v95, v98, v95
	v_mov_b32_e32 v122, v119
	v_fma_f32 v95, v102, v95, v174
	v_pk_mul_f32 v[96:97], v[92:93], v[122:123]
	v_max_f32_e32 v173, 0, v95
	v_add_f32_e32 v95, v96, v97
	v_add_f32_e32 v95, v99, v95
	v_fmac_f32_e32 v175, v103, v95
	v_or_b32_e32 v95, 0x21fd0, v94
	v_or_b32_e32 v100, 0x221d0, v94
	ds_read_b128 v[96:99], v95
	ds_read_b128 v[100:103], v100
	v_or_b32_e32 v95, 0x223d0, v94
	v_or_b32_e32 v94, 0x225d0, v94
	ds_read_b128 v[116:119], v95
	ds_read_b128 v[120:123], v94
	s_waitcnt lgkmcnt(4)
	v_mov_b32_e32 v124, v176
	s_waitcnt lgkmcnt(3)
	v_mov_b32_e32 v125, v96
	v_pk_mul_f32 v[94:95], v[92:93], v[124:125]
	v_mov_b32_e32 v96, v177
	v_add_f32_e32 v94, v94, v95
	s_waitcnt lgkmcnt(2)
	v_add_f32_e32 v94, v100, v94
	s_waitcnt lgkmcnt(0)
	v_fma_f32 v94, v116, v94, v120
	v_max_f32_e32 v100, 0, v94
	v_pk_mul_f32 v[94:95], v[92:93], v[96:97]
	v_max_f32_e32 v174, 0, v175
	v_add_f32_e32 v94, v94, v95
	v_add_f32_e32 v94, v101, v94
	v_fma_f32 v94, v117, v94, v121
	v_max_f32_e32 v96, 0, v94
	v_mov_b32_e32 v94, v178
	v_mov_b32_e32 v95, v98
	v_mov_b32_e32 v98, v179
	v_pk_mul_f32 v[94:95], v[92:93], v[94:95]
	v_pk_mul_f32 v[92:93], v[92:93], v[98:99]
	v_add_f32_e32 v94, v94, v95
	v_add_f32_e32 v92, v92, v93
	v_add_f32_e32 v94, v102, v94
	v_add_f32_e32 v92, v103, v92
	v_fma_f32 v94, v118, v94, v122
	v_fmac_f32_e32 v123, v119, v92
	v_max_f32_e32 v94, 0, v94
	v_max_f32_e32 v92, 0, v123
	v_cvt_pk_f16_f32 v95, v94, v92
	v_cvt_pk_f16_f32 v94, v100, v96
	v_cvt_pk_f16_f32 v93, v173, v174
	v_cvt_pk_f16_f32 v92, v167, v172
	s_waitcnt vmcnt(16)
	v_cvt_f32_f16_sdwa v183, v163 dst_sel:DWORD dst_unused:UNUSED_PAD src0_sel:WORD_1
	v_cvt_f32_f16_e32 v182, v163
	v_cvt_f32_f16_sdwa v163, v127 dst_sel:DWORD dst_unused:UNUSED_PAD src0_sel:WORD_1
	v_cvt_f32_f16_sdwa v97, v90 dst_sel:DWORD dst_unused:UNUSED_PAD src0_sel:WORD_1
	v_cvt_f32_f16_e32 v96, v90
	v_mfma_f32_32x32x16_f16 v[48:63], v[104:107], v[92:95], v[48:63]
	v_cvt_f32_f16_sdwa v99, v88 dst_sel:DWORD dst_unused:UNUSED_PAD src0_sel:WORD_1
	v_cvt_f32_f16_e32 v98, v88
	v_or_b32_e32 v88, 0x23a00, v165
	v_cvt_f32_f16_sdwa v101, v89 dst_sel:DWORD dst_unused:UNUSED_PAD src0_sel:WORD_1
	v_cvt_f32_f16_e32 v100, v89
	v_pk_fma_f32 v[96:97], v[98:99], s[4:5], v[96:97] op_sel_hi:[1,0,1]
	v_cvt_f32_f16_sdwa v99, v91 dst_sel:DWORD dst_unused:UNUSED_PAD src0_sel:WORD_1
	v_mfma_f32_32x32x16_f16 v[32:47], v[108:111], v[92:95], v[32:47]
	v_cvt_f32_f16_e32 v98, v91
	v_mfma_f32_32x32x16_f16 v[16:31], v[112:115], v[92:95], v[16:31]
	v_mfma_f32_32x32x16_f16 v[0:15], v[168:171], v[92:95], v[0:15]
	ds_read_b128 v[92:95], v88
	v_or_b32_e32 v88, 0x23a20, v165
	ds_read_b128 v[88:91], v88
	s_waitcnt lgkmcnt(1)
	v_add_f32_e64 v48, v48, v92
	v_add_f32_e64 v49, v49, v93
	v_pk_add_f32 v[48:49], v[96:97], v[48:49]
	v_cvt_f32_f16_sdwa v93, v86 dst_sel:DWORD dst_unused:UNUSED_PAD src0_sel:WORD_1
	v_cvt_f32_f16_e32 v92, v86
	v_cvt_f32_f16_sdwa v97, v84 dst_sel:DWORD dst_unused:UNUSED_PAD src0_sel:WORD_1
	v_cvt_f32_f16_e32 v96, v84
	v_cvt_pk_f16_f32 v112, v48, v49
	v_pk_fma_f32 v[48:49], v[100:101], s[4:5], v[98:99] op_sel_hi:[1,0,1]
	v_pk_add_f32 v[50:51], v[50:51], v[94:95]
	v_cvt_f32_f16_e32 v86, v85
	v_pk_add_f32 v[48:49], v[48:49], v[50:51]
	v_cvt_f32_f16_sdwa v51, v87 dst_sel:DWORD dst_unused:UNUSED_PAD src0_sel:WORD_1
	v_cvt_f32_f16_e32 v50, v87
	v_cvt_f32_f16_sdwa v87, v85 dst_sel:DWORD dst_unused:UNUSED_PAD src0_sel:WORD_1
	v_cvt_pk_f16_f32 v113, v48, v49
	v_pk_fma_f32 v[48:49], v[96:97], s[4:5], v[92:93] op_sel_hi:[1,0,1]
	s_waitcnt lgkmcnt(0)
	v_pk_add_f32 v[52:53], v[52:53], v[88:89]
	s_nop 0
	v_pk_add_f32 v[48:49], v[48:49], v[52:53]
	v_cvt_f32_f16_sdwa v53, v82 dst_sel:DWORD dst_unused:UNUSED_PAD src0_sel:WORD_1
	v_cvt_pk_f16_f32 v114, v48, v49
	v_pk_fma_f32 v[48:49], v[86:87], s[4:5], v[50:51] op_sel_hi:[1,0,1]
	v_pk_add_f32 v[50:51], v[54:55], v[90:91]
	v_cvt_f32_f16_e32 v52, v82
	v_pk_add_f32 v[48:49], v[48:49], v[50:51]
	v_cvt_f32_f16_sdwa v55, v80 dst_sel:DWORD dst_unused:UNUSED_PAD src0_sel:WORD_1
	v_cvt_pk_f16_f32 v115, v48, v49
	v_or_b32_e32 v48, 0x23a40, v165
	v_cvt_f32_f16_e32 v54, v80
	ds_read_b128 v[48:51], v48
	v_cvt_f32_f16_sdwa v87, v83 dst_sel:DWORD dst_unused:UNUSED_PAD src0_sel:WORD_1
	v_cvt_f32_f16_e32 v86, v83
	v_cvt_f32_f16_sdwa v83, v81 dst_sel:DWORD dst_unused:UNUSED_PAD src0_sel:WORD_1
	v_cvt_f32_f16_e32 v82, v81
	v_pk_fma_f32 v[84:85], v[54:55], s[4:5], v[52:53] op_sel_hi:[1,0,1]
	v_or_b32_e32 v52, 0x23a60, v165
	ds_read_b128 v[52:55], v52
	s_waitcnt lgkmcnt(1)
	v_pk_add_f32 v[48:49], v[56:57], v[48:49]
	v_cvt_f32_f16_sdwa v57, v78 dst_sel:DWORD dst_unused:UNUSED_PAD src0_sel:WORD_1
	v_cvt_f32_f16_e32 v56, v78
	v_cvt_f32_f16_sdwa v81, v76 dst_sel:DWORD dst_unused:UNUSED_PAD src0_sel:WORD_1
	v_cvt_f32_f16_e32 v80, v76
	v_pk_add_f32 v[48:49], v[84:85], v[48:49]
	v_pk_add_f32 v[50:51], v[58:59], v[50:51]
	v_cvt_pk_f16_f32 v116, v48, v49
	v_pk_fma_f32 v[48:49], v[82:83], s[4:5], v[86:87] op_sel_hi:[1,0,1]
	s_waitcnt lgkmcnt(0)
	v_pk_add_f32 v[52:53], v[60:61], v[52:53]
	v_pk_add_f32 v[48:49], v[48:49], v[50:51]
	v_cvt_f32_f16_sdwa v51, v79 dst_sel:DWORD dst_unused:UNUSED_PAD src0_sel:WORD_1
	v_cvt_pk_f16_f32 v117, v48, v49
	v_pk_fma_f32 v[48:49], v[80:81], s[4:5], v[56:57] op_sel_hi:[1,0,1]
	v_cvt_f32_f16_e32 v50, v79
	v_cvt_f32_f16_sdwa v57, v77 dst_sel:DWORD dst_unused:UNUSED_PAD src0_sel:WORD_1
	v_cvt_f32_f16_e32 v56, v77
	v_pk_add_f32 v[48:49], v[48:49], v[52:53]
	v_cvt_f32_f16_sdwa v53, v74 dst_sel:DWORD dst_unused:UNUSED_PAD src0_sel:WORD_1
	v_cvt_pk_f16_f32 v118, v48, v49
	v_pk_fma_f32 v[48:49], v[56:57], s[4:5], v[50:51] op_sel_hi:[1,0,1]
	v_pk_add_f32 v[50:51], v[62:63], v[54:55]
	v_cvt_f32_f16_e32 v52, v74
	v_pk_add_f32 v[48:49], v[48:49], v[50:51]
	v_cvt_f32_f16_sdwa v55, v72 dst_sel:DWORD dst_unused:UNUSED_PAD src0_sel:WORD_1
	v_cvt_pk_f16_f32 v119, v48, v49
	v_or_b32_e32 v48, 0x23a80, v165
	v_cvt_f32_f16_e32 v54, v72
	ds_read_b128 v[48:51], v48
	v_cvt_f32_f16_sdwa v59, v75 dst_sel:DWORD dst_unused:UNUSED_PAD src0_sel:WORD_1
	v_cvt_f32_f16_e32 v58, v75
	v_pk_fma_f32 v[56:57], v[54:55], s[4:5], v[52:53] op_sel_hi:[1,0,1]
	v_cvt_f32_f16_sdwa v61, v73 dst_sel:DWORD dst_unused:UNUSED_PAD src0_sel:WORD_1
	v_cvt_f32_f16_e32 v60, v73
	v_or_b32_e32 v52, 0x23aa0, v165
	ds_read_b128 v[52:55], v52
	s_waitcnt lgkmcnt(1)
	v_pk_add_f32 v[32:33], v[32:33], v[48:49]
	v_cvt_f32_f16_sdwa v49, v70 dst_sel:DWORD dst_unused:UNUSED_PAD src0_sel:WORD_1
	v_pk_add_f32 v[32:33], v[56:57], v[32:33]
	v_cvt_f32_f16_e32 v48, v70
	v_cvt_f32_f16_sdwa v57, v68 dst_sel:DWORD dst_unused:UNUSED_PAD src0_sel:WORD_1
	v_cvt_f32_f16_e32 v56, v68
	v_cvt_pk_f16_f32 v120, v32, v33
	v_pk_fma_f32 v[32:33], v[60:61], s[4:5], v[58:59] op_sel_hi:[1,0,1]
	v_pk_add_f32 v[34:35], v[34:35], v[50:51]
	s_waitcnt lgkmcnt(0)
	v_pk_add_f32 v[36:37], v[36:37], v[52:53]
	v_pk_add_f32 v[32:33], v[32:33], v[34:35]
	v_cvt_f32_f16_sdwa v35, v71 dst_sel:DWORD dst_unused:UNUSED_PAD src0_sel:WORD_1
	v_cvt_pk_f16_f32 v121, v32, v33
	v_pk_fma_f32 v[32:33], v[56:57], s[4:5], v[48:49] op_sel_hi:[1,0,1]
	v_cvt_f32_f16_e32 v34, v71
	v_cvt_f32_f16_sdwa v49, v69 dst_sel:DWORD dst_unused:UNUSED_PAD src0_sel:WORD_1
	v_cvt_f32_f16_e32 v48, v69
	v_pk_add_f32 v[32:33], v[32:33], v[36:37]
	v_cvt_f32_f16_sdwa v37, v66 dst_sel:DWORD dst_unused:UNUSED_PAD src0_sel:WORD_1
	v_cvt_pk_f16_f32 v122, v32, v33
	v_pk_fma_f32 v[32:33], v[48:49], s[4:5], v[34:35] op_sel_hi:[1,0,1]
	v_pk_add_f32 v[34:35], v[38:39], v[54:55]
	v_cvt_f32_f16_e32 v36, v66
	v_cvt_f32_f16_sdwa v39, v64 dst_sel:DWORD dst_unused:UNUSED_PAD src0_sel:WORD_1
	v_cvt_f32_f16_e32 v38, v64
	v_pk_add_f32 v[32:33], v[32:33], v[34:35]
	v_or_b32_e32 v48, 0x23ac0, v165
	v_cvt_pk_f16_f32 v123, v32, v33
	v_pk_fma_f32 v[32:33], v[38:39], s[4:5], v[36:37] op_sel_hi:[1,0,1]
	ds_read_b128 v[36:39], v166 offset:34816
	v_cvt_f32_f16_sdwa v35, v67 dst_sel:DWORD dst_unused:UNUSED_PAD src0_sel:WORD_1
	v_cvt_f32_f16_e32 v34, v67
	v_cvt_f32_f16_sdwa v57, v65 dst_sel:DWORD dst_unused:UNUSED_PAD src0_sel:WORD_1
	v_cvt_f32_f16_e32 v56, v65
	v_or_b32_e32 v52, 0x23ae0, v165
	ds_read_b128 v[48:51], v48
	ds_read_b128 v[168:171], v52
	ds_read_b128 v[52:55], v166 offset:43520
	ds_read_b128 v[172:175], v166 offset:34848
	s_waitcnt lgkmcnt(4)
	v_mfma_f32_32x32x16_f16 v[96:111], v[36:39], v[112:115], 0
	s_waitcnt lgkmcnt(3)
	v_add_f32_e64 v36, v40, v48
	v_add_f32_e64 v37, v41, v49
	v_fma_f32 v40, v56, s4, v34
	v_fma_f32 v41, v57, s4, v35
	v_pk_add_f32 v[32:33], v[32:33], v[36:37]
	v_pk_add_f32 v[42:43], v[42:43], v[50:51]
	v_cvt_pk_f16_f32 v124, v32, v33
	ds_read_b128 v[32:35], v166 offset:52224
	ds_read_b128 v[36:39], v166 offset:43552
	v_pk_add_f32 v[48:49], v[40:41], v[42:43]
	s_waitcnt lgkmcnt(3)
	v_mfma_f32_32x32x16_f16 v[80:95], v[52:55], v[112:115], 0
	v_cvt_f32_f16_sdwa v51, v162 dst_sel:DWORD dst_unused:UNUSED_PAD src0_sel:WORD_1
	v_cvt_f32_f16_e32 v50, v162
	v_cvt_f32_f16_sdwa v53, v126 dst_sel:DWORD dst_unused:UNUSED_PAD src0_sel:WORD_1
	v_cvt_f32_f16_e32 v52, v126
	ds_read_b128 v[40:43], v166 offset:60928
	ds_read_b128 v[176:179], v166 offset:52256
	v_cvt_f32_f16_e32 v162, v127
	v_cvt_pk_f16_f32 v125, v48, v49
	v_pk_fma_f32 v[180:181], v[52:53], s[4:5], v[50:51] op_sel_hi:[1,0,1]
	s_waitcnt lgkmcnt(1)
	v_mfma_f32_32x32x16_f16 v[48:63], v[40:43], v[112:115], 0
	v_add_f32_e64 v40, v44, v168
	v_add_f32_e64 v41, v45, v169
	v_add_f32_e64 v42, v46, v170
	v_add_f32_e64 v43, v47, v171
	v_add_f32_e64 v40, v180, v40
	v_add_f32_e64 v41, v181, v41
	s_waitcnt vmcnt(15)
	v_cvt_f32_f16_sdwa v45, v160 dst_sel:DWORD dst_unused:UNUSED_PAD src0_sel:WORD_1
	v_cvt_pk_f16_f32 v126, v40, v41
	v_pk_fma_f32 v[40:41], v[162:163], s[4:5], v[182:183] op_sel_hi:[1,0,1]
	v_cvt_f32_f16_e32 v44, v160
	v_pk_add_f32 v[40:41], v[40:41], v[42:43]
	s_waitcnt vmcnt(14)
	v_cvt_f32_f16_sdwa v47, v128 dst_sel:DWORD dst_unused:UNUSED_PAD src0_sel:WORD_1
	v_cvt_pk_f16_f32 v127, v40, v41
	v_or_b32_e32 v40, 0x23b00, v165
	ds_read_b128 v[40:43], v40
	v_cvt_f32_f16_e32 v46, v128
	v_mfma_f32_32x32x16_f16 v[64:79], v[32:35], v[112:115], 0
	ds_read_b128 v[32:35], v166 offset:60960
	s_waitcnt vmcnt(13)
	v_cvt_f32_f16_e32 v160, v130
	v_fma_f32 v44, v46, s4, v44
	v_fma_f32 v45, v47, s4, v45
	v_cvt_f32_f16_sdwa v47, v129 dst_sel:DWORD dst_unused:UNUSED_PAD src0_sel:WORD_1
	v_cvt_f32_f16_e32 v46, v129
	v_mfma_f32_32x32x16_f16 v[80:95], v[36:39], v[116:119], v[80:95]
	v_or_b32_e32 v36, 0x23b20, v165
	ds_read_b128 v[36:39], v36
	s_waitcnt lgkmcnt(2)
	v_add_f32_e64 v16, v16, v40
	v_add_f32_e64 v17, v17, v41
	v_cvt_f32_f16_sdwa v41, v161 dst_sel:DWORD dst_unused:UNUSED_PAD src0_sel:WORD_1
	v_cvt_f32_f16_e32 v40, v161
	v_pk_add_f32 v[16:17], v[44:45], v[16:17]
	v_pk_add_f32 v[18:19], v[18:19], v[42:43]
	v_cvt_pk_f16_f32 v128, v16, v17
	v_pk_fma_f32 v[16:17], v[46:47], s[4:5], v[40:41] op_sel_hi:[1,0,1]
	ds_read_b128 v[44:47], v166 offset:34880
	v_mfma_f32_32x32x16_f16 v[96:111], v[172:175], v[116:119], v[96:111]
	s_waitcnt vmcnt(12)
	v_cvt_f32_f16_sdwa v41, v158 dst_sel:DWORD dst_unused:UNUSED_PAD src0_sel:WORD_1
	v_cvt_f32_f16_e32 v40, v158
	v_cvt_f32_f16_sdwa v161, v130 dst_sel:DWORD dst_unused:UNUSED_PAD src0_sel:WORD_1
	v_add_f32_e64 v16, v16, v18
	v_add_f32_e64 v17, v17, v19
	s_waitcnt lgkmcnt(1)
	v_pk_add_f32 v[20:21], v[20:21], v[36:37]
	v_cvt_pk_f16_f32 v129, v16, v17
	v_cvt_f32_f16_sdwa v37, v159 dst_sel:DWORD dst_unused:UNUSED_PAD src0_sel:WORD_1
	v_mfma_f32_32x32x16_f16 v[48:63], v[32:35], v[116:119], v[48:63]
	ds_read_b128 v[16:19], v166 offset:43584
	ds_read_b128 v[32:35], v166 offset:34912
	v_cvt_f32_f16_e32 v36, v159
	v_cvt_f32_f16_sdwa v159, v131 dst_sel:DWORD dst_unused:UNUSED_PAD src0_sel:WORD_1
	v_cvt_f32_f16_e32 v158, v131
	v_pk_fma_f32 v[160:161], v[160:161], s[4:5], v[40:41] op_sel_hi:[1,0,1]
	v_mfma_f32_32x32x16_f16 v[64:79], v[176:179], v[116:119], v[64:79]
	s_waitcnt lgkmcnt(1)
	v_mfma_f32_32x32x16_f16 v[80:95], v[16:19], v[120:123], v[80:95]
	v_add_f32_e64 v16, v160, v20
	v_add_f32_e64 v17, v161, v21
	v_add_f32_e64 v18, v22, v38
	v_add_f32_e64 v19, v23, v39
	v_cvt_pk_f16_f32 v130, v16, v17
	v_pk_fma_f32 v[16:17], v[158:159], s[4:5], v[36:37] op_sel_hi:[1,0,1]
	s_nop 0
	v_pk_add_f32 v[36:37], v[16:17], v[18:19]
	v_mfma_f32_32x32x16_f16 v[96:111], v[44:47], v[120:123], v[96:111]
	ds_read_b128 v[40:43], v166 offset:52288
	ds_read_b128 v[44:47], v166 offset:43616
	ds_read_b128 v[16:19], v166 offset:60992
	ds_read_b128 v[20:23], v166 offset:52320
	v_cvt_pk_f16_f32 v131, v36, v37
	ds_read_b128 v[36:39], v166 offset:61024
	s_waitcnt lgkmcnt(4)
	v_mfma_f32_32x32x16_f16 v[64:79], v[40:43], v[120:123], v[64:79]
	s_waitcnt vmcnt(10)
	v_cvt_f32_f16_sdwa v43, v132 dst_sel:DWORD dst_unused:UNUSED_PAD src0_sel:WORD_1
	v_cvt_f32_f16_e32 v42, v132
	v_or_b32_e32 v132, 0x23b40, v165
	v_cvt_f32_f16_sdwa v41, v156 dst_sel:DWORD dst_unused:UNUSED_PAD src0_sel:WORD_1
	v_cvt_f32_f16_e32 v40, v156
	v_cvt_f32_f16_e32 v156, v133
	v_pk_fma_f32 v[40:41], v[42:43], s[4:5], v[40:41] op_sel_hi:[1,0,1]
	s_waitcnt lgkmcnt(2)
	v_mfma_f32_32x32x16_f16 v[48:63], v[16:19], v[120:123], v[48:63]
	ds_read_b128 v[16:19], v132
	v_cvt_f32_f16_sdwa v43, v157 dst_sel:DWORD dst_unused:UNUSED_PAD src0_sel:WORD_1
	v_cvt_f32_f16_e32 v42, v157
	v_cvt_f32_f16_sdwa v157, v133 dst_sel:DWORD dst_unused:UNUSED_PAD src0_sel:WORD_1
	v_or_b32_e32 v132, 0x23b60, v165
	s_waitcnt lgkmcnt(0)
	v_pk_add_f32 v[16:17], v[24:25], v[16:17]
	s_waitcnt vmcnt(8)
	v_cvt_f32_f16_sdwa v25, v154 dst_sel:DWORD dst_unused:UNUSED_PAD src0_sel:WORD_1
	v_mfma_f32_32x32x16_f16 v[96:111], v[32:35], v[124:127], v[96:111]
	ds_read_b128 v[32:35], v132
	v_add_f32_e64 v16, v40, v16
	v_add_f32_e64 v17, v41, v17
	v_cvt_f32_f16_e32 v24, v154
	v_cvt_f32_f16_sdwa v41, v134 dst_sel:DWORD dst_unused:UNUSED_PAD src0_sel:WORD_1
	v_cvt_f32_f16_e32 v40, v134
	v_cvt_pk_f16_f32 v132, v16, v17
	v_pk_fma_f32 v[16:17], v[156:157], s[4:5], v[42:43] op_sel_hi:[1,0,1]
	v_pk_add_f32 v[18:19], v[26:27], v[18:19]
	v_mfma_f32_32x32x16_f16 v[80:95], v[44:47], v[124:127], v[80:95]
	v_add_f32_e64 v16, v16, v18
	v_add_f32_e64 v17, v17, v19
	s_waitcnt lgkmcnt(0)
	v_add_f32_e64 v18, v28, v32
	v_add_f32_e64 v19, v29, v33
	v_cvt_pk_f16_f32 v133, v16, v17
	v_pk_fma_f32 v[16:17], v[40:41], s[4:5], v[24:25] op_sel_hi:[1,0,1]
	v_pk_add_f32 v[30:31], v[30:31], v[34:35]
	v_pk_add_f32 v[16:17], v[16:17], v[18:19]
	s_waitcnt vmcnt(7)
	v_cvt_f32_f16_sdwa v33, v152 dst_sel:DWORD dst_unused:UNUSED_PAD src0_sel:WORD_1
	v_cvt_pk_f16_f32 v134, v16, v17
	ds_read_b128 v[16:19], v166 offset:34944
	v_mfma_f32_32x32x16_f16 v[64:79], v[20:23], v[124:127], v[64:79]
	v_cvt_f32_f16_sdwa v21, v155 dst_sel:DWORD dst_unused:UNUSED_PAD src0_sel:WORD_1
	v_cvt_f32_f16_e32 v20, v155
	v_cvt_f32_f16_sdwa v23, v135 dst_sel:DWORD dst_unused:UNUSED_PAD src0_sel:WORD_1
	v_cvt_f32_f16_e32 v22, v135
	v_cvt_f32_f16_e32 v32, v152
	s_waitcnt vmcnt(6)
	v_cvt_f32_f16_sdwa v35, v136 dst_sel:DWORD dst_unused:UNUSED_PAD src0_sel:WORD_1
	v_cvt_f32_f16_e32 v34, v136
	v_pk_fma_f32 v[28:29], v[22:23], s[4:5], v[20:21] op_sel_hi:[1,0,1]
	ds_read_b128 v[20:23], v166 offset:43648
	ds_read_b128 v[24:27], v166 offset:34976
	s_waitcnt lgkmcnt(2)
	v_mfma_f32_32x32x16_f16 v[96:111], v[16:19], v[128:131], v[96:111]
	v_add_f32_e64 v16, v28, v30
	v_add_f32_e64 v17, v29, v31
	v_fma_f32 v40, v34, s4, v32
	v_fma_f32 v41, v35, s4, v33
	v_cvt_pk_f16_f32 v135, v16, v17
	ds_read_b128 v[16:19], v166 offset:52352
	ds_read_b128 v[28:31], v166 offset:43680
	v_cvt_f32_f16_sdwa v43, v153 dst_sel:DWORD dst_unused:UNUSED_PAD src0_sel:WORD_1
	v_cvt_f32_f16_e32 v42, v153
	v_cvt_f32_f16_sdwa v45, v137 dst_sel:DWORD dst_unused:UNUSED_PAD src0_sel:WORD_1
	v_mfma_f32_32x32x16_f16 v[48:63], v[36:39], v[124:127], v[48:63]
	v_or_b32_e32 v36, 0x23b80, v165
	v_cvt_f32_f16_e32 v44, v137
	s_waitcnt lgkmcnt(3)
	v_mfma_f32_32x32x16_f16 v[80:95], v[20:23], v[128:131], v[80:95]
	ds_read_b128 v[20:23], v36
	ds_read_b128 v[32:35], v166 offset:61056
	ds_read_b128 v[36:39], v166 offset:52384
	s_waitcnt lgkmcnt(2)
	v_add_f32_e64 v0, v0, v20
	v_add_f32_e64 v1, v1, v21
	v_pk_add_f32 v[0:1], v[40:41], v[0:1]
	v_mfma_f32_32x32x16_f16 v[64:79], v[16:19], v[128:131], v[64:79]
	v_or_b32_e32 v16, 0x23ba0, v165
	ds_read_b128 v[16:19], v16
	v_add_f32_e64 v2, v2, v22
	v_add_f32_e64 v3, v3, v23
	s_waitcnt vmcnt(4)
	v_cvt_f32_f16_sdwa v21, v150 dst_sel:DWORD dst_unused:UNUSED_PAD src0_sel:WORD_1
	v_cvt_f32_f16_e32 v20, v150
	v_cvt_f32_f16_sdwa v23, v138 dst_sel:DWORD dst_unused:UNUSED_PAD src0_sel:WORD_1
	v_cvt_f32_f16_e32 v22, v138
	v_cvt_pk_f16_f32 v136, v0, v1
	v_pk_fma_f32 v[0:1], v[44:45], s[4:5], v[42:43] op_sel_hi:[1,0,1]
	ds_read_b128 v[40:43], v166 offset:61088
	v_pk_add_f32 v[0:1], v[0:1], v[2:3]
	s_waitcnt lgkmcnt(1)
	v_pk_add_f32 v[2:3], v[4:5], v[16:17]
	v_cvt_f32_f16_sdwa v5, v151 dst_sel:DWORD dst_unused:UNUSED_PAD src0_sel:WORD_1
	v_cvt_f32_f16_e32 v4, v151
	v_cvt_f32_f16_sdwa v17, v139 dst_sel:DWORD dst_unused:UNUSED_PAD src0_sel:WORD_1
	v_cvt_f32_f16_e32 v16, v139
	v_cvt_pk_f16_f32 v137, v0, v1
	v_pk_fma_f32 v[0:1], v[22:23], s[4:5], v[20:21] op_sel_hi:[1,0,1]
	v_mfma_f32_32x32x16_f16 v[48:63], v[32:35], v[128:131], v[48:63]
	v_add_f32_e64 v0, v0, v2
	v_add_f32_e64 v1, v1, v3
	v_add_f32_e64 v2, v6, v18
	v_add_f32_e64 v3, v7, v19
	v_cvt_pk_f16_f32 v138, v0, v1
	v_pk_fma_f32 v[0:1], v[16:17], s[4:5], v[4:5] op_sel_hi:[1,0,1]
	s_waitcnt vmcnt(3)
	v_cvt_f32_f16_sdwa v5, v148 dst_sel:DWORD dst_unused:UNUSED_PAD src0_sel:WORD_1
	v_pk_add_f32 v[0:1], v[0:1], v[2:3]
	v_cvt_f32_f16_e32 v4, v148
	v_cvt_pk_f16_f32 v139, v0, v1
	ds_read_b128 v[0:3], v166 offset:35008
	v_mfma_f32_32x32x16_f16 v[96:111], v[24:27], v[132:135], v[96:111]
	s_waitcnt vmcnt(2)
	v_cvt_f32_f16_sdwa v7, v140 dst_sel:DWORD dst_unused:UNUSED_PAD src0_sel:WORD_1
	v_cvt_f32_f16_e32 v6, v140
	v_or_b32_e32 v16, 0x23bc0, v165
	v_or_b32_e32 v17, 0x23be0, v165
	v_cvt_f32_f16_sdwa v33, v141 dst_sel:DWORD dst_unused:UNUSED_PAD src0_sel:WORD_1
	v_cvt_f32_f16_e32 v32, v141
	v_mfma_f32_32x32x16_f16 v[80:95], v[28:31], v[132:135], v[80:95]
	v_fma_f32 v28, v6, s4, v4
	v_fma_f32 v29, v7, s4, v5
	v_cvt_f32_f16_sdwa v31, v149 dst_sel:DWORD dst_unused:UNUSED_PAD src0_sel:WORD_1
	v_cvt_f32_f16_e32 v30, v149
	ds_read_b128 v[4:7], v16
	ds_read_b128 v[16:19], v17
	ds_read_b128 v[20:23], v166 offset:43712
	ds_read_b128 v[24:27], v166 offset:35040
	s_waitcnt lgkmcnt(3)
	v_pk_add_f32 v[10:11], v[10:11], v[6:7]
	v_mfma_f32_32x32x16_f16 v[64:79], v[36:39], v[132:135], v[64:79]
	v_mfma_f32_32x32x16_f16 v[48:63], v[40:43], v[132:135], v[48:63]
	v_mfma_f32_32x32x16_f16 v[96:111], v[0:3], v[136:139], v[96:111]
	v_add_f32_e64 v0, v8, v4
	v_add_f32_e64 v1, v9, v5
	v_fma_f32 v8, v32, s4, v30
	v_fma_f32 v9, v33, s4, v31
	v_add_f32_e64 v0, v28, v0
	v_add_f32_e64 v1, v29, v1
	v_pk_add_f32 v[28:29], v[8:9], v[10:11]
	v_cvt_pk_f16_f32 v140, v0, v1
	ds_read_b128 v[0:3], v166 offset:52416
	ds_read_b128 v[4:7], v166 offset:43744
	s_waitcnt vmcnt(0)
	v_cvt_f32_f16_sdwa v31, v146 dst_sel:DWORD dst_unused:UNUSED_PAD src0_sel:WORD_1
	s_waitcnt lgkmcnt(3)
	v_mfma_f32_32x32x16_f16 v[80:95], v[20:23], v[136:139], v[80:95]
	ds_read_b128 v[8:11], v166 offset:61120
	ds_read_b128 v[20:23], v166 offset:52448
	v_cvt_f32_f16_e32 v30, v146
	v_cvt_f32_f16_sdwa v33, v142 dst_sel:DWORD dst_unused:UNUSED_PAD src0_sel:WORD_1
	v_cvt_f32_f16_e32 v32, v142
	v_cvt_pk_f16_f32 v141, v28, v29
	v_lshlrev_b32_e32 v146, 2, v164
	v_pk_fma_f32 v[28:29], v[32:33], s[4:5], v[30:31] op_sel_hi:[1,0,1]
	s_waitcnt lgkmcnt(3)
	v_mfma_f32_32x32x16_f16 v[64:79], v[0:3], v[136:139], v[64:79]
	ds_read_b128 v[0:3], v166 offset:61152
	v_cvt_f32_f16_sdwa v31, v147 dst_sel:DWORD dst_unused:UNUSED_PAD src0_sel:WORD_1
	v_cvt_f32_f16_e32 v30, v147
	v_cvt_f32_f16_sdwa v33, v143 dst_sel:DWORD dst_unused:UNUSED_PAD src0_sel:WORD_1
	v_cvt_f32_f16_e32 v32, v143
	v_lshlrev_b32_e32 v147, 2, v146
	s_waitcnt lgkmcnt(2)
	v_mfma_f32_32x32x16_f16 v[48:63], v[8:11], v[136:139], v[48:63]
	v_add_f32_e64 v8, v12, v16
	v_add_f32_e64 v9, v13, v17
	v_add_f32_e64 v10, v14, v18
	v_add_f32_e64 v11, v15, v19
	v_add_f32_e64 v8, v28, v8
	v_add_f32_e64 v9, v29, v9
	v_cvt_pk_f16_f32 v142, v8, v9
	v_pk_fma_f32 v[8:9], v[32:33], s[4:5], v[30:31] op_sel_hi:[1,0,1]
	s_load_dwordx4 s[4:7], s[0:1], 0x1f0
	v_pk_add_f32 v[8:9], v[8:9], v[10:11]
	s_nop 0
	v_cvt_pk_f16_f32 v143, v8, v9
	s_nop 1
	v_mfma_f32_32x32x16_f16 v[96:111], v[24:27], v[140:143], v[96:111]
	v_mfma_f32_32x32x16_f16 v[80:95], v[4:7], v[140:143], v[80:95]
	v_mul_u32_u24_e32 v4, 0x110, v145
	v_ashrrev_i32_e32 v145, 31, v144
	s_waitcnt lgkmcnt(0)
	v_mfma_f32_32x32x16_f16 v[64:79], v[20:23], v[140:143], v[64:79]
	v_mfma_f32_32x32x16_f16 v[48:63], v[0:3], v[140:143], v[48:63]
	s_and_saveexec_b64 s[0:1], s[8:9]
	s_cbranch_execz .LBB12_28
	v_or_b32_e32 v0, 0x23600, v147
	ds_read_b128 v[6:9], v0
	v_or_b32_e32 v2, 0x23620, v147
	ds_read_b128 v[10:13], v2
	v_lshlrev_b64 v[0:1], 5, v[144:145]
	v_lshl_add_u64 v[0:1], s[4:5], 0, v[0:1]
	s_waitcnt lgkmcnt(1)
	v_pk_add_f32 v[2:3], v[96:97], v[6:7]
	s_lshl_b64 s[4:5], s[36:37], 20
	v_cvt_pk_f16_f32 v6, v2, v3
	v_pk_add_f32 v[2:3], v[98:99], v[8:9]
	v_lshl_add_u64 v[8:9], v[0:1], 0, s[4:5]
	v_cvt_pk_f16_f32 v7, v2, v3
	v_lshlrev_b32_e32 v2, 1, v146
	v_mov_b32_e32 v3, 0
	v_lshl_add_u64 v[14:15], v[8:9], 0, v[2:3]
	global_store_dwordx2 v[14:15], v[6:7], off
	s_waitcnt lgkmcnt(0)
	v_pk_add_f32 v[6:7], v[100:101], v[10:11]
	v_or_b32_e32 v5, 0x23640, v147
	v_cvt_pk_f16_f32 v10, v6, v7
	ds_read_b128 v[6:9], v5
	v_pk_add_f32 v[12:13], v[102:103], v[12:13]
	v_or_b32_e32 v5, 0x23660, v147
	v_cvt_pk_f16_f32 v11, v12, v13
	global_store_dwordx2 v[14:15], v[10:11], off offset:16
	ds_read_b128 v[10:13], v5
	s_waitcnt lgkmcnt(1)
	v_pk_add_f32 v[6:7], v[104:105], v[6:7]
	v_pk_add_f32 v[8:9], v[106:107], v[8:9]
	s_lshl_b64 s[4:5], s[34:35], 20
	v_cvt_pk_f16_f32 v6, v6, v7
	v_cvt_pk_f16_f32 v7, v8, v9
	v_lshl_add_u64 v[8:9], v[0:1], 0, s[4:5]
	v_lshl_add_u64 v[14:15], v[8:9], 0, v[2:3]
	global_store_dwordx2 v[14:15], v[6:7], off
	s_waitcnt lgkmcnt(0)
	v_pk_add_f32 v[6:7], v[108:109], v[10:11]
	v_or_b32_e32 v5, 0x23680, v147
	v_cvt_pk_f16_f32 v10, v6, v7
	ds_read_b128 v[6:9], v5
	v_pk_add_f32 v[12:13], v[110:111], v[12:13]
	v_or_b32_e32 v5, 0x236a0, v147
	v_cvt_pk_f16_f32 v11, v12, v13
	global_store_dwordx2 v[14:15], v[10:11], off offset:16
	ds_read_b128 v[10:13], v5
	s_waitcnt lgkmcnt(1)
	v_pk_add_f32 v[6:7], v[80:81], v[6:7]
	v_pk_add_f32 v[8:9], v[82:83], v[8:9]
	s_lshl_b64 s[4:5], s[30:31], 20
	v_cvt_pk_f16_f32 v6, v6, v7
	v_cvt_pk_f16_f32 v7, v8, v9
	v_lshl_add_u64 v[8:9], v[0:1], 0, s[4:5]
	v_lshl_add_u64 v[14:15], v[8:9], 0, v[2:3]
	global_store_dwordx2 v[14:15], v[6:7], off
	s_waitcnt lgkmcnt(0)
	v_pk_add_f32 v[6:7], v[84:85], v[10:11]
	v_or_b32_e32 v5, 0x236c0, v147
	v_cvt_pk_f16_f32 v10, v6, v7
	ds_read_b128 v[6:9], v5
	v_pk_add_f32 v[12:13], v[86:87], v[12:13]
	v_or_b32_e32 v5, 0x236e0, v147
	v_cvt_pk_f16_f32 v11, v12, v13
	global_store_dwordx2 v[14:15], v[10:11], off offset:16
	ds_read_b128 v[10:13], v5
	s_waitcnt lgkmcnt(1)
	v_pk_add_f32 v[6:7], v[88:89], v[6:7]
	v_pk_add_f32 v[8:9], v[90:91], v[8:9]
	s_lshl_b64 s[4:5], s[28:29], 20
	v_cvt_pk_f16_f32 v6, v6, v7
	v_cvt_pk_f16_f32 v7, v8, v9
	v_lshl_add_u64 v[8:9], v[0:1], 0, s[4:5]
	v_lshl_add_u64 v[14:15], v[8:9], 0, v[2:3]
	global_store_dwordx2 v[14:15], v[6:7], off
	s_waitcnt lgkmcnt(0)
	v_pk_add_f32 v[6:7], v[92:93], v[10:11]
	v_or_b32_e32 v5, 0x23700, v147
	v_cvt_pk_f16_f32 v10, v6, v7
	ds_read_b128 v[6:9], v5
	v_pk_add_f32 v[12:13], v[94:95], v[12:13]
	v_or_b32_e32 v5, 0x23720, v147
	v_cvt_pk_f16_f32 v11, v12, v13
	global_store_dwordx2 v[14:15], v[10:11], off offset:16
	ds_read_b128 v[10:13], v5
	s_waitcnt lgkmcnt(1)
	v_pk_add_f32 v[6:7], v[64:65], v[6:7]
	v_pk_add_f32 v[8:9], v[66:67], v[8:9]
	s_lshl_b64 s[4:5], s[26:27], 20
	v_cvt_pk_f16_f32 v6, v6, v7
	v_cvt_pk_f16_f32 v7, v8, v9
	v_lshl_add_u64 v[8:9], v[0:1], 0, s[4:5]
	v_lshl_add_u64 v[14:15], v[8:9], 0, v[2:3]
	global_store_dwordx2 v[14:15], v[6:7], off
	s_waitcnt lgkmcnt(0)
	v_pk_add_f32 v[6:7], v[68:69], v[10:11]
	v_or_b32_e32 v5, 0x23740, v147
	v_cvt_pk_f16_f32 v10, v6, v7
	ds_read_b128 v[6:9], v5
	v_pk_add_f32 v[12:13], v[70:71], v[12:13]
	v_or_b32_e32 v5, 0x23760, v147
	v_cvt_pk_f16_f32 v11, v12, v13
	global_store_dwordx2 v[14:15], v[10:11], off offset:16
	ds_read_b128 v[10:13], v5
	s_waitcnt lgkmcnt(1)
	v_pk_add_f32 v[6:7], v[72:73], v[6:7]
	v_pk_add_f32 v[8:9], v[74:75], v[8:9]
	s_lshl_b64 s[4:5], s[24:25], 20
	v_cvt_pk_f16_f32 v6, v6, v7
	v_cvt_pk_f16_f32 v7, v8, v9
	v_lshl_add_u64 v[8:9], v[0:1], 0, s[4:5]
	v_lshl_add_u64 v[14:15], v[8:9], 0, v[2:3]
	global_store_dwordx2 v[14:15], v[6:7], off
	s_waitcnt lgkmcnt(0)
	v_pk_add_f32 v[6:7], v[76:77], v[10:11]
	v_or_b32_e32 v5, 0x23780, v147
	v_cvt_pk_f16_f32 v10, v6, v7
	ds_read_b128 v[6:9], v5
	v_pk_add_f32 v[12:13], v[78:79], v[12:13]
	v_or_b32_e32 v5, 0x237a0, v147
	v_cvt_pk_f16_f32 v11, v12, v13
	global_store_dwordx2 v[14:15], v[10:11], off offset:16
	ds_read_b128 v[10:13], v5
	s_waitcnt lgkmcnt(1)
	v_pk_add_f32 v[6:7], v[48:49], v[6:7]
	v_pk_add_f32 v[8:9], v[50:51], v[8:9]
	s_lshl_b64 s[4:5], s[10:11], 20
	v_cvt_pk_f16_f32 v6, v6, v7
	v_cvt_pk_f16_f32 v7, v8, v9
	v_lshl_add_u64 v[8:9], v[0:1], 0, s[4:5]
	v_lshl_add_u64 v[14:15], v[8:9], 0, v[2:3]
	global_store_dwordx2 v[14:15], v[6:7], off
	s_waitcnt lgkmcnt(0)
	v_pk_add_f32 v[6:7], v[52:53], v[10:11]
	v_or_b32_e32 v5, 0x237c0, v147
	v_cvt_pk_f16_f32 v10, v6, v7
	v_pk_add_f32 v[12:13], v[54:55], v[12:13]
	ds_read_b128 v[6:9], v5
	v_cvt_pk_f16_f32 v11, v12, v13
	v_or_b32_e32 v5, 0x237e0, v147
	global_store_dwordx2 v[14:15], v[10:11], off offset:16
	ds_read_b128 v[10:13], v5
	s_lshl_b64 s[4:5], s[2:3], 20
	s_waitcnt lgkmcnt(1)
	v_pk_add_f32 v[6:7], v[56:57], v[6:7]
	v_pk_add_f32 v[8:9], v[58:59], v[8:9]
	v_lshl_add_u64 v[0:1], v[0:1], 0, s[4:5]
	v_cvt_pk_f16_f32 v6, v6, v7
	v_cvt_pk_f16_f32 v7, v8, v9
	v_lshl_add_u64 v[0:1], v[0:1], 0, v[2:3]
	global_store_dwordx2 v[0:1], v[6:7], off
	s_waitcnt lgkmcnt(0)
	v_pk_add_f32 v[2:3], v[60:61], v[10:11]
	v_pk_add_f32 v[6:7], v[62:63], v[12:13]
	v_cvt_pk_f16_f32 v2, v2, v3
	v_cvt_pk_f16_f32 v3, v6, v7
	global_store_dwordx2 v[0:1], v[2:3], off offset:16
